# c11
# baseline (speedup 1.0000x reference)
.LBB2_3:
	s_add_i32 s44, s62, 0xfffff000
	s_and_b32 s44, s44, 0x1000
	ds_read_b128 v[202:205], v175
	ds_read_b128 v[206:209], v175 offset:256
	ds_read_b128 v[210:213], v175 offset:512
	ds_read_b128 v[214:217], v175 offset:768
	ds_read_b128 v[218:221], v175 offset:1024
	ds_read_b128 v[222:225], v175 offset:1280
	ds_read_b128 v[226:229], v175 offset:1536
	ds_read_b128 v[230:233], v175 offset:1792
	ds_read2_b64 v[178:181], v171 offset1:1
	ds_read2_b64 v[182:185], v171 offset0:2 offset1:48
	ds_read2_b64 v[186:189], v171 offset0:49 offset1:50
	s_mov_b32 m0, s59
	ds_read2_b64 v[190:193], v171 offset0:96 offset1:97
	global_load_lds_dwordx4 v144, s[76:77]
	s_mov_b32 m0, s58
	ds_read2_b64 v[194:197], v171 offset0:98 offset1:144
	global_load_lds_dwordx4 v145, s[76:77]
	s_mov_b32 m0, s57
	ds_read2_b64 v[198:201], v171 offset0:145 offset1:146
	global_load_lds_dwordx4 v146, s[76:77]
	v_add_u32_e32 v152, s44, v176
	ds_read_u16 v240, v152
	ds_read_u16 v241, v152 offset:32
	ds_read_u16 v242, v152 offset:64
	s_add_i32 s44, s62, 0xfffff800
	s_and_b32 s44, s44, 0x1800
	s_add_i32 m0, s50, s44
	ds_read_u16 v243, v152 offset:96
	global_load_lds_dword v150, s[80:81]
	s_waitcnt vmcnt(6)
	s_waitcnt lgkmcnt(0)
	s_barrier
	v_mfma_scale_f32_16x16x128_f8f6f4 v[126:129], v[202:205], v[178:183], v[126:129], v177, v240 op_sel_hi:[0,0,0] cbsz:4 blgp:2
	v_mfma_scale_f32_16x16x128_f8f6f4 v[122:125], v[206:209], v[178:183], v[122:125], v177, v240 op_sel_hi:[0,0,0] cbsz:4 blgp:2
	v_mfma_scale_f32_16x16x128_f8f6f4 v[114:117], v[210:213], v[178:183], v[114:117], v177, v240 op_sel_hi:[0,0,0] cbsz:4 blgp:2
	v_mfma_scale_f32_16x16x128_f8f6f4 v[102:105], v[214:217], v[178:183], v[102:105], v177, v240 op_sel_hi:[0,0,0] cbsz:4 blgp:2
	v_mfma_scale_f32_16x16x128_f8f6f4 v[86:89], v[218:221], v[178:183], v[86:89], v177, v240 op_sel_hi:[0,0,0] cbsz:4 blgp:2
	v_mfma_scale_f32_16x16x128_f8f6f4 v[70:73], v[222:225], v[178:183], v[70:73], v177, v240 op_sel_hi:[0,0,0] cbsz:4 blgp:2
	v_mfma_scale_f32_16x16x128_f8f6f4 v[54:57], v[226:229], v[178:183], v[54:57], v177, v240 op_sel_hi:[0,0,0] cbsz:4 blgp:2
	v_mfma_scale_f32_16x16x128_f8f6f4 v[38:41], v[230:233], v[178:183], v[38:41], v177, v240 op_sel_hi:[0,0,0] cbsz:4 blgp:2
	v_mfma_scale_f32_16x16x128_f8f6f4 v[118:121], v[202:205], v[184:189], v[118:121], v177, v241 op_sel_hi:[0,0,0] cbsz:4 blgp:2
	v_mfma_scale_f32_16x16x128_f8f6f4 v[110:113], v[206:209], v[184:189], v[110:113], v177, v241 op_sel_hi:[0,0,0] cbsz:4 blgp:2
	v_mfma_scale_f32_16x16x128_f8f6f4 v[98:101], v[210:213], v[184:189], v[98:101], v177, v241 op_sel_hi:[0,0,0] cbsz:4 blgp:2
	v_mfma_scale_f32_16x16x128_f8f6f4 v[82:85], v[214:217], v[184:189], v[82:85], v177, v241 op_sel_hi:[0,0,0] cbsz:4 blgp:2
	v_mfma_scale_f32_16x16x128_f8f6f4 v[66:69], v[218:221], v[184:189], v[66:69], v177, v241 op_sel_hi:[0,0,0] cbsz:4 blgp:2
	v_mfma_scale_f32_16x16x128_f8f6f4 v[50:53], v[222:225], v[184:189], v[50:53], v177, v241 op_sel_hi:[0,0,0] cbsz:4 blgp:2
	v_mfma_scale_f32_16x16x128_f8f6f4 v[34:37], v[226:229], v[184:189], v[34:37], v177, v241 op_sel_hi:[0,0,0] cbsz:4 blgp:2
	v_mfma_scale_f32_16x16x128_f8f6f4 v[106:109], v[202:205], v[190:195], v[106:109], v177, v242 op_sel_hi:[0,0,0] cbsz:4 blgp:2
	v_mfma_scale_f32_16x16x128_f8f6f4 v[94:97], v[206:209], v[190:195], v[94:97], v177, v242 op_sel_hi:[0,0,0] cbsz:4 blgp:2
	v_mfma_scale_f32_16x16x128_f8f6f4 v[78:81], v[210:213], v[190:195], v[78:81], v177, v242 op_sel_hi:[0,0,0] cbsz:4 blgp:2
	v_mfma_scale_f32_16x16x128_f8f6f4 v[62:65], v[214:217], v[190:195], v[62:65], v177, v242 op_sel_hi:[0,0,0] cbsz:4 blgp:2
	v_mfma_scale_f32_16x16x128_f8f6f4 v[46:49], v[218:221], v[190:195], v[46:49], v177, v242 op_sel_hi:[0,0,0] cbsz:4 blgp:2
	v_mfma_scale_f32_16x16x128_f8f6f4 v[30:33], v[222:225], v[190:195], v[30:33], v177, v242 op_sel_hi:[0,0,0] cbsz:4 blgp:2
	v_mfma_scale_f32_16x16x128_f8f6f4 v[90:93], v[202:205], v[196:201], v[90:93], v177, v243 op_sel_hi:[0,0,0] cbsz:4 blgp:2
	v_mfma_scale_f32_16x16x128_f8f6f4 v[74:77], v[206:209], v[196:201], v[74:77], v177, v243 op_sel_hi:[0,0,0] cbsz:4 blgp:2
	v_mfma_scale_f32_16x16x128_f8f6f4 v[58:61], v[210:213], v[196:201], v[58:61], v177, v243 op_sel_hi:[0,0,0] cbsz:4 blgp:2
	v_mfma_scale_f32_16x16x128_f8f6f4 v[42:45], v[214:217], v[196:201], v[42:45], v177, v243 op_sel_hi:[0,0,0] cbsz:4 blgp:2
	v_mfma_scale_f32_16x16x128_f8f6f4 v[26:29], v[218:221], v[196:201], v[26:29], v177, v243 op_sel_hi:[0,0,0] cbsz:4 blgp:2
	v_mfma_scale_f32_16x16x128_f8f6f4 v[178:181], v[230:233], v[184:189], v[22:25], v177, v241 op_sel_hi:[0,0,0] cbsz:4 blgp:2
	v_mfma_scale_f32_16x16x128_f8f6f4 v[182:185], v[226:229], v[190:195], v[18:21], v177, v242 op_sel_hi:[0,0,0] cbsz:4 blgp:2
	v_mfma_scale_f32_16x16x128_f8f6f4 v[186:189], v[230:233], v[190:195], v[10:13], v177, v242 op_sel_hi:[0,0,0] cbsz:4 blgp:2
	v_mfma_scale_f32_16x16x128_f8f6f4 v[190:193], v[222:225], v[196:201], v[14:17], v177, v243 op_sel_hi:[0,0,0] cbsz:4 blgp:2
	v_mfma_scale_f32_16x16x128_f8f6f4 v[234:237], v[226:229], v[196:201], v[6:9], v177, v243 op_sel_hi:[0,0,0] cbsz:4 blgp:2
	v_mfma_scale_f32_16x16x128_f8f6f4 v[194:197], v[230:233], v[196:201], v[2:5], v177, v243 op_sel_hi:[0,0,0] cbsz:4 blgp:2
	s_barrier
	ds_read2_b64 v[2:5], v167 offset1:1
	s_mov_b32 m0, s54
	ds_read2_b64 v[6:9], v167 offset0:2 offset1:48
	global_load_lds_dwordx4 v147, s[76:77]
	s_mov_b32 m0, s52
	ds_read2_b64 v[10:13], v167 offset0:49 offset1:50
	global_load_lds_dwordx4 v148, s[76:77]
	s_mov_b32 m0, s51
	ds_read2_b64 v[14:17], v167 offset0:96 offset1:97
	global_load_lds_dwordx4 v149, s[76:77]
	s_mov_b32 m0, s15
	ds_read2_b64 v[18:21], v167 offset0:98 offset1:144
	global_load_lds_dwordx4 v142, s[72:73]
	s_mov_b32 m0, s46
	ds_read2_b64 v[22:25], v167 offset0:145 offset1:146
	global_load_lds_dwordx4 v143, s[72:73]
	s_waitcnt vmcnt(5)
	s_waitcnt lgkmcnt(0)
	s_barrier
	v_mfma_scale_f32_16x16x128_f8f6f4 v[126:129], v[202:205], v[2:7], v[126:129], v177, v240 op_sel:[0,1,0] op_sel_hi:[0,0,0] cbsz:4 blgp:2
	v_mfma_scale_f32_16x16x128_f8f6f4 v[122:125], v[206:209], v[2:7], v[122:125], v177, v240 op_sel:[0,1,0] op_sel_hi:[0,0,0] cbsz:4 blgp:2
	v_mfma_scale_f32_16x16x128_f8f6f4 v[114:117], v[210:213], v[2:7], v[114:117], v177, v240 op_sel:[0,1,0] op_sel_hi:[0,0,0] cbsz:4 blgp:2
	v_mfma_scale_f32_16x16x128_f8f6f4 v[102:105], v[214:217], v[2:7], v[102:105], v177, v240 op_sel:[0,1,0] op_sel_hi:[0,0,0] cbsz:4 blgp:2
	v_mfma_scale_f32_16x16x128_f8f6f4 v[86:89], v[218:221], v[2:7], v[86:89], v177, v240 op_sel:[0,1,0] op_sel_hi:[0,0,0] cbsz:4 blgp:2
	v_mfma_scale_f32_16x16x128_f8f6f4 v[70:73], v[222:225], v[2:7], v[70:73], v177, v240 op_sel:[0,1,0] op_sel_hi:[0,0,0] cbsz:4 blgp:2
	v_mfma_scale_f32_16x16x128_f8f6f4 v[54:57], v[226:229], v[2:7], v[54:57], v177, v240 op_sel:[0,1,0] op_sel_hi:[0,0,0] cbsz:4 blgp:2
	v_mfma_scale_f32_16x16x128_f8f6f4 v[38:41], v[230:233], v[2:7], v[38:41], v177, v240 op_sel:[0,1,0] op_sel_hi:[0,0,0] cbsz:4 blgp:2
	v_mfma_scale_f32_16x16x128_f8f6f4 v[118:121], v[202:205], v[8:13], v[118:121], v177, v241 op_sel:[0,1,0] op_sel_hi:[0,0,0] cbsz:4 blgp:2
	v_mfma_scale_f32_16x16x128_f8f6f4 v[110:113], v[206:209], v[8:13], v[110:113], v177, v241 op_sel:[0,1,0] op_sel_hi:[0,0,0] cbsz:4 blgp:2
	v_mfma_scale_f32_16x16x128_f8f6f4 v[98:101], v[210:213], v[8:13], v[98:101], v177, v241 op_sel:[0,1,0] op_sel_hi:[0,0,0] cbsz:4 blgp:2
	v_mfma_scale_f32_16x16x128_f8f6f4 v[82:85], v[214:217], v[8:13], v[82:85], v177, v241 op_sel:[0,1,0] op_sel_hi:[0,0,0] cbsz:4 blgp:2
	v_mfma_scale_f32_16x16x128_f8f6f4 v[66:69], v[218:221], v[8:13], v[66:69], v177, v241 op_sel:[0,1,0] op_sel_hi:[0,0,0] cbsz:4 blgp:2
	v_mfma_scale_f32_16x16x128_f8f6f4 v[50:53], v[222:225], v[8:13], v[50:53], v177, v241 op_sel:[0,1,0] op_sel_hi:[0,0,0] cbsz:4 blgp:2
	v_mfma_scale_f32_16x16x128_f8f6f4 v[34:37], v[226:229], v[8:13], v[34:37], v177, v241 op_sel:[0,1,0] op_sel_hi:[0,0,0] cbsz:4 blgp:2
	v_mfma_scale_f32_16x16x128_f8f6f4 v[106:109], v[202:205], v[14:19], v[106:109], v177, v242 op_sel:[0,1,0] op_sel_hi:[0,0,0] cbsz:4 blgp:2
	v_mfma_scale_f32_16x16x128_f8f6f4 v[94:97], v[206:209], v[14:19], v[94:97], v177, v242 op_sel:[0,1,0] op_sel_hi:[0,0,0] cbsz:4 blgp:2
	v_mfma_scale_f32_16x16x128_f8f6f4 v[78:81], v[210:213], v[14:19], v[78:81], v177, v242 op_sel:[0,1,0] op_sel_hi:[0,0,0] cbsz:4 blgp:2
	v_mfma_scale_f32_16x16x128_f8f6f4 v[62:65], v[214:217], v[14:19], v[62:65], v177, v242 op_sel:[0,1,0] op_sel_hi:[0,0,0] cbsz:4 blgp:2
	v_mfma_scale_f32_16x16x128_f8f6f4 v[46:49], v[218:221], v[14:19], v[46:49], v177, v242 op_sel:[0,1,0] op_sel_hi:[0,0,0] cbsz:4 blgp:2
	v_mfma_scale_f32_16x16x128_f8f6f4 v[30:33], v[222:225], v[14:19], v[30:33], v177, v242 op_sel:[0,1,0] op_sel_hi:[0,0,0] cbsz:4 blgp:2
	v_mfma_scale_f32_16x16x128_f8f6f4 v[90:93], v[202:205], v[20:25], v[90:93], v177, v243 op_sel:[0,1,0] op_sel_hi:[0,0,0] cbsz:4 blgp:2
	v_mfma_scale_f32_16x16x128_f8f6f4 v[74:77], v[206:209], v[20:25], v[74:77], v177, v243 op_sel:[0,1,0] op_sel_hi:[0,0,0] cbsz:4 blgp:2
	v_mfma_scale_f32_16x16x128_f8f6f4 v[58:61], v[210:213], v[20:25], v[58:61], v177, v243 op_sel:[0,1,0] op_sel_hi:[0,0,0] cbsz:4 blgp:2
	v_mfma_scale_f32_16x16x128_f8f6f4 v[42:45], v[214:217], v[20:25], v[42:45], v177, v243 op_sel:[0,1,0] op_sel_hi:[0,0,0] cbsz:4 blgp:2
	v_mfma_scale_f32_16x16x128_f8f6f4 v[26:29], v[218:221], v[20:25], v[26:29], v177, v243 op_sel:[0,1,0] op_sel_hi:[0,0,0] cbsz:4 blgp:2
	v_mfma_scale_f32_16x16x128_f8f6f4 v[178:181], v[230:233], v[8:13], v[178:181], v177, v241 op_sel:[0,1,0] op_sel_hi:[0,0,0] cbsz:4 blgp:2
	v_mfma_scale_f32_16x16x128_f8f6f4 v[182:185], v[226:229], v[14:19], v[182:185], v177, v242 op_sel:[0,1,0] op_sel_hi:[0,0,0] cbsz:4 blgp:2
	v_mfma_scale_f32_16x16x128_f8f6f4 v[186:189], v[230:233], v[14:19], v[186:189], v177, v242 op_sel:[0,1,0] op_sel_hi:[0,0,0] cbsz:4 blgp:2
	v_mfma_scale_f32_16x16x128_f8f6f4 v[190:193], v[222:225], v[20:25], v[190:193], v177, v243 op_sel:[0,1,0] op_sel_hi:[0,0,0] cbsz:4 blgp:2
	v_mfma_scale_f32_16x16x128_f8f6f4 v[198:201], v[226:229], v[20:25], v[234:237], v177, v243 op_sel:[0,1,0] op_sel_hi:[0,0,0] cbsz:4 blgp:2
	v_mfma_scale_f32_16x16x128_f8f6f4 v[194:197], v[230:233], v[20:25], v[194:197], v177, v243 op_sel:[0,1,0] op_sel_hi:[0,0,0] cbsz:4 blgp:2
	s_barrier
	ds_read_b128 v[202:205], v166
	ds_read_b128 v[206:209], v166 offset:256
	ds_read_b128 v[210:213], v166 offset:512
	ds_read_b128 v[214:217], v166 offset:768
	ds_read_b128 v[218:221], v166 offset:1024
	ds_read_b128 v[222:225], v166 offset:1280
	ds_read_b128 v[226:229], v166 offset:1536
	ds_read_b128 v[230:233], v166 offset:1792
	ds_read2_b64 v[2:5], v162 offset1:1
	ds_read2_b64 v[6:9], v162 offset0:2 offset1:48
	ds_read2_b64 v[10:13], v162 offset0:49 offset1:50
	s_mov_b32 m0, s47
	ds_read2_b64 v[14:17], v162 offset0:96 offset1:97
	global_load_lds_dwordx4 v144, s[78:79]
	s_mov_b32 m0, s48
	ds_read2_b64 v[18:21], v162 offset0:98 offset1:144
	global_load_lds_dwordx4 v145, s[78:79]
	s_mov_b32 m0, s49
	ds_read2_b64 v[22:25], v162 offset0:145 offset1:146
	global_load_lds_dwordx4 v146, s[78:79]
	v_add_u32_e32 v234, s44, v176
	ds_read_u16 v242, v234
	ds_read_u16 v243, v234 offset:32
	ds_read_u16 v244, v234 offset:64
	s_and_b32 s44, s62, 0x1000
	s_add_i32 m0, s50, s44
	ds_read_u16 v245, v234 offset:96
	global_load_lds_dword v151, s[80:81]
	s_waitcnt vmcnt(6)
	s_waitcnt lgkmcnt(0)
	s_barrier
	v_mfma_scale_f32_16x16x128_f8f6f4 v[126:129], v[202:205], v[2:7], v[126:129], v177, v242 op_sel_hi:[0,0,0] cbsz:4 blgp:2
	v_mfma_scale_f32_16x16x128_f8f6f4 v[122:125], v[206:209], v[2:7], v[122:125], v177, v242 op_sel_hi:[0,0,0] cbsz:4 blgp:2
	v_mfma_scale_f32_16x16x128_f8f6f4 v[114:117], v[210:213], v[2:7], v[114:117], v177, v242 op_sel_hi:[0,0,0] cbsz:4 blgp:2
	v_mfma_scale_f32_16x16x128_f8f6f4 v[102:105], v[214:217], v[2:7], v[102:105], v177, v242 op_sel_hi:[0,0,0] cbsz:4 blgp:2
	v_mfma_scale_f32_16x16x128_f8f6f4 v[86:89], v[218:221], v[2:7], v[86:89], v177, v242 op_sel_hi:[0,0,0] cbsz:4 blgp:2
	v_mfma_scale_f32_16x16x128_f8f6f4 v[70:73], v[222:225], v[2:7], v[70:73], v177, v242 op_sel_hi:[0,0,0] cbsz:4 blgp:2
	v_mfma_scale_f32_16x16x128_f8f6f4 v[54:57], v[226:229], v[2:7], v[54:57], v177, v242 op_sel_hi:[0,0,0] cbsz:4 blgp:2
	v_mfma_scale_f32_16x16x128_f8f6f4 v[38:41], v[230:233], v[2:7], v[38:41], v177, v242 op_sel_hi:[0,0,0] cbsz:4 blgp:2
	v_mfma_scale_f32_16x16x128_f8f6f4 v[118:121], v[202:205], v[8:13], v[118:121], v177, v243 op_sel_hi:[0,0,0] cbsz:4 blgp:2
	v_mfma_scale_f32_16x16x128_f8f6f4 v[110:113], v[206:209], v[8:13], v[110:113], v177, v243 op_sel_hi:[0,0,0] cbsz:4 blgp:2
	v_mfma_scale_f32_16x16x128_f8f6f4 v[98:101], v[210:213], v[8:13], v[98:101], v177, v243 op_sel_hi:[0,0,0] cbsz:4 blgp:2
	v_mfma_scale_f32_16x16x128_f8f6f4 v[82:85], v[214:217], v[8:13], v[82:85], v177, v243 op_sel_hi:[0,0,0] cbsz:4 blgp:2
	v_mfma_scale_f32_16x16x128_f8f6f4 v[66:69], v[218:221], v[8:13], v[66:69], v177, v243 op_sel_hi:[0,0,0] cbsz:4 blgp:2
	v_mfma_scale_f32_16x16x128_f8f6f4 v[50:53], v[222:225], v[8:13], v[50:53], v177, v243 op_sel_hi:[0,0,0] cbsz:4 blgp:2
	v_mfma_scale_f32_16x16x128_f8f6f4 v[34:37], v[226:229], v[8:13], v[34:37], v177, v243 op_sel_hi:[0,0,0] cbsz:4 blgp:2
	v_mfma_scale_f32_16x16x128_f8f6f4 v[106:109], v[202:205], v[14:19], v[106:109], v177, v244 op_sel_hi:[0,0,0] cbsz:4 blgp:2
	v_mfma_scale_f32_16x16x128_f8f6f4 v[94:97], v[206:209], v[14:19], v[94:97], v177, v244 op_sel_hi:[0,0,0] cbsz:4 blgp:2
	v_mfma_scale_f32_16x16x128_f8f6f4 v[78:81], v[210:213], v[14:19], v[78:81], v177, v244 op_sel_hi:[0,0,0] cbsz:4 blgp:2
	v_mfma_scale_f32_16x16x128_f8f6f4 v[62:65], v[214:217], v[14:19], v[62:65], v177, v244 op_sel_hi:[0,0,0] cbsz:4 blgp:2
	v_mfma_scale_f32_16x16x128_f8f6f4 v[46:49], v[218:221], v[14:19], v[46:49], v177, v244 op_sel_hi:[0,0,0] cbsz:4 blgp:2
	v_mfma_scale_f32_16x16x128_f8f6f4 v[30:33], v[222:225], v[14:19], v[30:33], v177, v244 op_sel_hi:[0,0,0] cbsz:4 blgp:2
	v_mfma_scale_f32_16x16x128_f8f6f4 v[238:241], v[226:229], v[14:19], v[182:185], v177, v244 op_sel_hi:[0,0,0] cbsz:4 blgp:2
	v_mfma_scale_f32_16x16x128_f8f6f4 v[14:17], v[230:233], v[14:19], v[186:189], v177, v244 op_sel_hi:[0,0,0] cbsz:4 blgp:2
	v_mfma_scale_f32_16x16x128_f8f6f4 v[90:93], v[202:205], v[20:25], v[90:93], v177, v245 op_sel_hi:[0,0,0] cbsz:4 blgp:2
	v_mfma_scale_f32_16x16x128_f8f6f4 v[74:77], v[206:209], v[20:25], v[74:77], v177, v245 op_sel_hi:[0,0,0] cbsz:4 blgp:2
	v_mfma_scale_f32_16x16x128_f8f6f4 v[58:61], v[210:213], v[20:25], v[58:61], v177, v245 op_sel_hi:[0,0,0] cbsz:4 blgp:2
	v_mfma_scale_f32_16x16x128_f8f6f4 v[42:45], v[214:217], v[20:25], v[42:45], v177, v245 op_sel_hi:[0,0,0] cbsz:4 blgp:2
	v_mfma_scale_f32_16x16x128_f8f6f4 v[26:29], v[218:221], v[20:25], v[26:29], v177, v245 op_sel_hi:[0,0,0] cbsz:4 blgp:2
	v_mfma_scale_f32_16x16x128_f8f6f4 v[234:237], v[230:233], v[8:13], v[178:181], v177, v243 op_sel_hi:[0,0,0] cbsz:4 blgp:2
	v_mfma_scale_f32_16x16x128_f8f6f4 v[190:193], v[222:225], v[20:25], v[190:193], v177, v245 op_sel_hi:[0,0,0] cbsz:4 blgp:2
	v_mfma_scale_f32_16x16x128_f8f6f4 v[198:201], v[226:229], v[20:25], v[198:201], v177, v245 op_sel_hi:[0,0,0] cbsz:4 blgp:2
	v_mfma_scale_f32_16x16x128_f8f6f4 v[194:197], v[230:233], v[20:25], v[194:197], v177, v245 op_sel_hi:[0,0,0] cbsz:4 blgp:2
	s_barrier
	ds_read2_b64 v[2:5], v1 offset1:1
	s_mov_b32 m0, s53
	ds_read2_b64 v[6:9], v1 offset0:2 offset1:48
	global_load_lds_dwordx4 v147, s[78:79]
	s_mov_b32 m0, s55
	ds_read2_b64 v[10:13], v1 offset0:49 offset1:50
	global_load_lds_dwordx4 v148, s[78:79]
	s_mov_b32 m0, s56
	ds_read2_b64 v[178:181], v159 offset1:1
	global_load_lds_dwordx4 v149, s[78:79]
	s_mov_b32 m0, s63
	ds_read2_b64 v[182:185], v159 offset0:2 offset1:48
	global_load_lds_dwordx4 v142, s[74:75]
	s_mov_b32 m0, s60
	ds_read2_b64 v[186:189], v159 offset0:49 offset1:50
	global_load_lds_dwordx4 v143, s[74:75]
	s_waitcnt vmcnt(5)
	s_waitcnt lgkmcnt(0)
	s_barrier
	v_mfma_scale_f32_16x16x128_f8f6f4 v[126:129], v[202:205], v[2:7], v[126:129], v177, v242 op_sel:[0,1,0] op_sel_hi:[0,0,0] cbsz:4 blgp:2
	v_mfma_scale_f32_16x16x128_f8f6f4 v[122:125], v[206:209], v[2:7], v[122:125], v177, v242 op_sel:[0,1,0] op_sel_hi:[0,0,0] cbsz:4 blgp:2
	v_mfma_scale_f32_16x16x128_f8f6f4 v[114:117], v[210:213], v[2:7], v[114:117], v177, v242 op_sel:[0,1,0] op_sel_hi:[0,0,0] cbsz:4 blgp:2
	v_mfma_scale_f32_16x16x128_f8f6f4 v[102:105], v[214:217], v[2:7], v[102:105], v177, v242 op_sel:[0,1,0] op_sel_hi:[0,0,0] cbsz:4 blgp:2
	v_mfma_scale_f32_16x16x128_f8f6f4 v[86:89], v[218:221], v[2:7], v[86:89], v177, v242 op_sel:[0,1,0] op_sel_hi:[0,0,0] cbsz:4 blgp:2
	v_mfma_scale_f32_16x16x128_f8f6f4 v[70:73], v[222:225], v[2:7], v[70:73], v177, v242 op_sel:[0,1,0] op_sel_hi:[0,0,0] cbsz:4 blgp:2
	v_mfma_scale_f32_16x16x128_f8f6f4 v[54:57], v[226:229], v[2:7], v[54:57], v177, v242 op_sel:[0,1,0] op_sel_hi:[0,0,0] cbsz:4 blgp:2
	v_mfma_scale_f32_16x16x128_f8f6f4 v[38:41], v[230:233], v[2:7], v[38:41], v177, v242 op_sel:[0,1,0] op_sel_hi:[0,0,0] cbsz:4 blgp:2
	v_mfma_scale_f32_16x16x128_f8f6f4 v[118:121], v[202:205], v[8:13], v[118:121], v177, v243 op_sel:[0,1,0] op_sel_hi:[0,0,0] cbsz:4 blgp:2
	v_mfma_scale_f32_16x16x128_f8f6f4 v[110:113], v[206:209], v[8:13], v[110:113], v177, v243 op_sel:[0,1,0] op_sel_hi:[0,0,0] cbsz:4 blgp:2
	v_mfma_scale_f32_16x16x128_f8f6f4 v[98:101], v[210:213], v[8:13], v[98:101], v177, v243 op_sel:[0,1,0] op_sel_hi:[0,0,0] cbsz:4 blgp:2
	v_mfma_scale_f32_16x16x128_f8f6f4 v[82:85], v[214:217], v[8:13], v[82:85], v177, v243 op_sel:[0,1,0] op_sel_hi:[0,0,0] cbsz:4 blgp:2
	v_mfma_scale_f32_16x16x128_f8f6f4 v[66:69], v[218:221], v[8:13], v[66:69], v177, v243 op_sel:[0,1,0] op_sel_hi:[0,0,0] cbsz:4 blgp:2
	v_mfma_scale_f32_16x16x128_f8f6f4 v[50:53], v[222:225], v[8:13], v[50:53], v177, v243 op_sel:[0,1,0] op_sel_hi:[0,0,0] cbsz:4 blgp:2
	v_mfma_scale_f32_16x16x128_f8f6f4 v[34:37], v[226:229], v[8:13], v[34:37], v177, v243 op_sel:[0,1,0] op_sel_hi:[0,0,0] cbsz:4 blgp:2
	v_mfma_scale_f32_16x16x128_f8f6f4 v[22:25], v[230:233], v[8:13], v[234:237], v177, v243 op_sel:[0,1,0] op_sel_hi:[0,0,0] cbsz:4 blgp:2
	v_mfma_scale_f32_16x16x128_f8f6f4 v[106:109], v[202:205], v[178:183], v[106:109], v177, v244 op_sel:[0,1,0] op_sel_hi:[0,0,0] cbsz:4 blgp:2
	v_mfma_scale_f32_16x16x128_f8f6f4 v[94:97], v[206:209], v[178:183], v[94:97], v177, v244 op_sel:[0,1,0] op_sel_hi:[0,0,0] cbsz:4 blgp:2
	v_mfma_scale_f32_16x16x128_f8f6f4 v[78:81], v[210:213], v[178:183], v[78:81], v177, v244 op_sel:[0,1,0] op_sel_hi:[0,0,0] cbsz:4 blgp:2
	v_mfma_scale_f32_16x16x128_f8f6f4 v[62:65], v[214:217], v[178:183], v[62:65], v177, v244 op_sel:[0,1,0] op_sel_hi:[0,0,0] cbsz:4 blgp:2
	v_mfma_scale_f32_16x16x128_f8f6f4 v[46:49], v[218:221], v[178:183], v[46:49], v177, v244 op_sel:[0,1,0] op_sel_hi:[0,0,0] cbsz:4 blgp:2
	v_mfma_scale_f32_16x16x128_f8f6f4 v[30:33], v[222:225], v[178:183], v[30:33], v177, v244 op_sel:[0,1,0] op_sel_hi:[0,0,0] cbsz:4 blgp:2
	v_mfma_scale_f32_16x16x128_f8f6f4 v[18:21], v[226:229], v[178:183], v[238:241], v177, v244 op_sel:[0,1,0] op_sel_hi:[0,0,0] cbsz:4 blgp:2
	v_mfma_scale_f32_16x16x128_f8f6f4 v[10:13], v[230:233], v[178:183], v[14:17], v177, v244 op_sel:[0,1,0] op_sel_hi:[0,0,0] cbsz:4 blgp:2
	v_mfma_scale_f32_16x16x128_f8f6f4 v[90:93], v[202:205], v[184:189], v[90:93], v177, v245 op_sel:[0,1,0] op_sel_hi:[0,0,0] cbsz:4 blgp:2
	v_mfma_scale_f32_16x16x128_f8f6f4 v[74:77], v[206:209], v[184:189], v[74:77], v177, v245 op_sel:[0,1,0] op_sel_hi:[0,0,0] cbsz:4 blgp:2
	v_mfma_scale_f32_16x16x128_f8f6f4 v[58:61], v[210:213], v[184:189], v[58:61], v177, v245 op_sel:[0,1,0] op_sel_hi:[0,0,0] cbsz:4 blgp:2
	v_mfma_scale_f32_16x16x128_f8f6f4 v[42:45], v[214:217], v[184:189], v[42:45], v177, v245 op_sel:[0,1,0] op_sel_hi:[0,0,0] cbsz:4 blgp:2
	v_mfma_scale_f32_16x16x128_f8f6f4 v[26:29], v[218:221], v[184:189], v[26:29], v177, v245 op_sel:[0,1,0] op_sel_hi:[0,0,0] cbsz:4 blgp:2
	v_mfma_scale_f32_16x16x128_f8f6f4 v[14:17], v[222:225], v[184:189], v[190:193], v177, v245 op_sel:[0,1,0] op_sel_hi:[0,0,0] cbsz:4 blgp:2
	v_mfma_scale_f32_16x16x128_f8f6f4 v[6:9], v[226:229], v[184:189], v[198:201], v177, v245 op_sel:[0,1,0] op_sel_hi:[0,0,0] cbsz:4 blgp:2
	v_mfma_scale_f32_16x16x128_f8f6f4 v[2:5], v[230:233], v[184:189], v[194:197], v177, v245 op_sel:[0,1,0] op_sel_hi:[0,0,0] cbsz:4 blgp:2
	s_barrier
	s_add_i32 s61, s61, 2
	s_addk_i32 s62, 0x1000
	s_add_u32 s72, s72, 0x8000
	s_addc_u32 s73, s73, 0
	s_add_u32 s74, s74, 0x8000
	s_addc_u32 s75, s75, 0
	s_add_u32 s76, s76, 0x18000
	s_addc_u32 s77, s77, 0
	s_add_u32 s78, s78, 0x18000
	s_addc_u32 s79, s79, 0
	s_add_u32 s80, s80, 0x1000
	s_addc_u32 s81, s81, 0
	s_cmp_lt_u32 s61, 4
	s_cbranch_scc1 .LBB2_3
	s_mov_b32 m0, s59
	s_nop 0
	global_load_lds_dwordx4 v144, s[76:77]
	s_mov_b32 m0, s58
	s_nop 0
	global_load_lds_dwordx4 v145, s[76:77]
	s_mov_b32 m0, s57
	s_nop 0
	global_load_lds_dwordx4 v146, s[76:77]
	s_add_i32 m0, s3, 0x21800
	s_nop 0
	global_load_lds_dword v150, s[80:81]
	s_mov_b32 m0, s54
	s_nop 0
	global_load_lds_dwordx4 v147, s[76:77]
	s_mov_b32 m0, s52
	s_nop 0
	global_load_lds_dwordx4 v148, s[76:77]
	s_mov_b32 m0, s51
	s_nop 0
	global_load_lds_dwordx4 v149, s[76:77]
	ds_read_b128 v[154:157], v175
	ds_read_b128 v[186:189], v175 offset:256
	ds_read_b128 v[190:193], v175 offset:512
	ds_read_b128 v[194:197], v175 offset:768
	ds_read_b128 v[198:201], v175 offset:1024
	ds_read_b128 v[202:205], v175 offset:1280
	ds_read_b128 v[206:209], v175 offset:1536
	ds_read_b128 v[210:213], v175 offset:1792
	ds_read_b64 v[142:143], v171
	ds_read_b64 v[144:145], v171 offset:8
	ds_read_b64 v[146:147], v171 offset:16
	ds_read_b64 v[148:149], v174
	ds_read_b64 v[150:151], v174 offset:8
	ds_read_b64 v[152:153], v174 offset:16
	ds_read_b64 v[174:175], v173
	ds_read_b64 v[176:177], v173 offset:8
	ds_read_b64 v[178:179], v173 offset:16
	ds_read_b64 v[180:181], v172
	ds_read_b64 v[182:183], v172 offset:8
	ds_read_b64 v[184:185], v172 offset:16
	v_add_u32_e32 v171, 0x21000, v161
	ds_read_u16 v215, v171 offset:32
	ds_read_u16 v216, v171 offset:64
	ds_read_u16 v214, v171 offset:96
	ds_read_u16 v171, v171
	s_waitcnt vmcnt(9)
	s_waitcnt lgkmcnt(0)
	s_barrier
	v_mov_b32_e32 v240, 0x7f7f7f7f
	s_nop 1
	v_mfma_scale_f32_16x16x128_f8f6f4 v[126:129], v[154:157], v[142:147], v[126:129], v240, v171 op_sel_hi:[0,0,0] cbsz:4 blgp:2
	v_mfma_scale_f32_16x16x128_f8f6f4 v[122:125], v[186:189], v[142:147], v[122:125], v240, v171 op_sel_hi:[0,0,0] cbsz:4 blgp:2
	v_mfma_scale_f32_16x16x128_f8f6f4 v[114:117], v[190:193], v[142:147], v[114:117], v240, v171 op_sel_hi:[0,0,0] cbsz:4 blgp:2
	v_mfma_scale_f32_16x16x128_f8f6f4 v[102:105], v[194:197], v[142:147], v[102:105], v240, v171 op_sel_hi:[0,0,0] cbsz:4 blgp:2
	v_mfma_scale_f32_16x16x128_f8f6f4 v[86:89], v[198:201], v[142:147], v[86:89], v240, v171 op_sel_hi:[0,0,0] cbsz:4 blgp:2
	v_mfma_scale_f32_16x16x128_f8f6f4 v[70:73], v[202:205], v[142:147], v[70:73], v240, v171 op_sel_hi:[0,0,0] cbsz:4 blgp:2
	v_mfma_scale_f32_16x16x128_f8f6f4 v[54:57], v[206:209], v[142:147], v[54:57], v240, v171 op_sel_hi:[0,0,0] cbsz:4 blgp:2
	v_mfma_scale_f32_16x16x128_f8f6f4 v[38:41], v[210:213], v[142:147], v[38:41], v240, v171 op_sel_hi:[0,0,0] cbsz:4 blgp:2
	v_mfma_scale_f32_16x16x128_f8f6f4 v[118:121], v[154:157], v[148:153], v[118:121], v240, v215 op_sel_hi:[0,0,0] cbsz:4 blgp:2
	v_mfma_scale_f32_16x16x128_f8f6f4 v[110:113], v[186:189], v[148:153], v[110:113], v240, v215 op_sel_hi:[0,0,0] cbsz:4 blgp:2
	v_mfma_scale_f32_16x16x128_f8f6f4 v[98:101], v[190:193], v[148:153], v[98:101], v240, v215 op_sel_hi:[0,0,0] cbsz:4 blgp:2
	v_mfma_scale_f32_16x16x128_f8f6f4 v[82:85], v[194:197], v[148:153], v[82:85], v240, v215 op_sel_hi:[0,0,0] cbsz:4 blgp:2
	v_mfma_scale_f32_16x16x128_f8f6f4 v[66:69], v[198:201], v[148:153], v[66:69], v240, v215 op_sel_hi:[0,0,0] cbsz:4 blgp:2
	v_mfma_scale_f32_16x16x128_f8f6f4 v[50:53], v[202:205], v[148:153], v[50:53], v240, v215 op_sel_hi:[0,0,0] cbsz:4 blgp:2
	v_mfma_scale_f32_16x16x128_f8f6f4 v[138:141], v[210:213], v[148:153], v[22:25], v240, v215 op_sel_hi:[0,0,0] cbsz:4 blgp:2
	v_mfma_scale_f32_16x16x128_f8f6f4 v[106:109], v[154:157], v[174:179], v[106:109], v240, v216 op_sel_hi:[0,0,0] cbsz:4 blgp:2
	v_mfma_scale_f32_16x16x128_f8f6f4 v[94:97], v[186:189], v[174:179], v[94:97], v240, v216 op_sel_hi:[0,0,0] cbsz:4 blgp:2
	v_mfma_scale_f32_16x16x128_f8f6f4 v[78:81], v[190:193], v[174:179], v[78:81], v240, v216 op_sel_hi:[0,0,0] cbsz:4 blgp:2
	v_mfma_scale_f32_16x16x128_f8f6f4 v[62:65], v[194:197], v[174:179], v[62:65], v240, v216 op_sel_hi:[0,0,0] cbsz:4 blgp:2
	v_mfma_scale_f32_16x16x128_f8f6f4 v[46:49], v[198:201], v[174:179], v[46:49], v240, v216 op_sel_hi:[0,0,0] cbsz:4 blgp:2
	v_mfma_scale_f32_16x16x128_f8f6f4 v[30:33], v[202:205], v[174:179], v[30:33], v240, v216 op_sel_hi:[0,0,0] cbsz:4 blgp:2
	v_mfma_scale_f32_16x16x128_f8f6f4 v[142:145], v[206:209], v[174:179], v[18:21], v240, v216 op_sel_hi:[0,0,0] cbsz:4 blgp:2
	v_mfma_scale_f32_16x16x128_f8f6f4 v[90:93], v[154:157], v[180:185], v[90:93], v240, v214 op_sel_hi:[0,0,0] cbsz:4 blgp:2
	v_mfma_scale_f32_16x16x128_f8f6f4 v[74:77], v[186:189], v[180:185], v[74:77], v240, v214 op_sel_hi:[0,0,0] cbsz:4 blgp:2
	v_mfma_scale_f32_16x16x128_f8f6f4 v[58:61], v[190:193], v[180:185], v[58:61], v240, v214 op_sel_hi:[0,0,0] cbsz:4 blgp:2
	v_mfma_scale_f32_16x16x128_f8f6f4 v[26:29], v[198:201], v[180:185], v[26:29], v240, v214 op_sel_hi:[0,0,0] cbsz:4 blgp:2
	v_mfma_scale_f32_16x16x128_f8f6f4 v[34:37], v[206:209], v[148:153], v[34:37], v240, v215 op_sel_hi:[0,0,0] cbsz:4 blgp:2
	v_mfma_scale_f32_16x16x128_f8f6f4 v[146:149], v[210:213], v[174:179], v[10:13], v240, v216 op_sel_hi:[0,0,0] cbsz:4 blgp:2
	v_mfma_scale_f32_16x16x128_f8f6f4 v[42:45], v[194:197], v[180:185], v[42:45], v240, v214 op_sel_hi:[0,0,0] cbsz:4 blgp:2
	v_mfma_scale_f32_16x16x128_f8f6f4 v[150:153], v[202:205], v[180:185], v[14:17], v240, v214 op_sel_hi:[0,0,0] cbsz:4 blgp:2
	v_mfma_scale_f32_16x16x128_f8f6f4 v[172:175], v[206:209], v[180:185], v[6:9], v240, v214 op_sel_hi:[0,0,0] cbsz:4 blgp:2
	v_mfma_scale_f32_16x16x128_f8f6f4 v[176:179], v[210:213], v[180:185], v[2:5], v240, v214 op_sel_hi:[0,0,0] cbsz:4 blgp:2
	s_barrier
	ds_read_b64 v[2:3], v167
	ds_read_b64 v[4:5], v167 offset:8
	ds_read_b64 v[6:7], v167 offset:16
	ds_read_b64 v[8:9], v170
	ds_read_b64 v[10:11], v170 offset:8
	ds_read_b64 v[12:13], v170 offset:16
	ds_read_b64 v[14:15], v169
	ds_read_b64 v[16:17], v169 offset:8
	ds_read_b64 v[18:19], v169 offset:16
	ds_read_b64 v[20:21], v168
	ds_read_b64 v[22:23], v168 offset:8
	ds_read_b64 v[24:25], v168 offset:16
	s_waitcnt vmcnt(3)
	s_waitcnt lgkmcnt(0)
	s_barrier
	v_mfma_scale_f32_16x16x128_f8f6f4 v[126:129], v[154:157], v[2:7], v[126:129], v240, v171 op_sel:[0,1,0] op_sel_hi:[0,0,0] cbsz:4 blgp:2
	v_mfma_scale_f32_16x16x128_f8f6f4 v[122:125], v[186:189], v[2:7], v[122:125], v240, v171 op_sel:[0,1,0] op_sel_hi:[0,0,0] cbsz:4 blgp:2
	v_mfma_scale_f32_16x16x128_f8f6f4 v[114:117], v[190:193], v[2:7], v[114:117], v240, v171 op_sel:[0,1,0] op_sel_hi:[0,0,0] cbsz:4 blgp:2
	v_mfma_scale_f32_16x16x128_f8f6f4 v[102:105], v[194:197], v[2:7], v[102:105], v240, v171 op_sel:[0,1,0] op_sel_hi:[0,0,0] cbsz:4 blgp:2
	v_mfma_scale_f32_16x16x128_f8f6f4 v[86:89], v[198:201], v[2:7], v[86:89], v240, v171 op_sel:[0,1,0] op_sel_hi:[0,0,0] cbsz:4 blgp:2
	v_mfma_scale_f32_16x16x128_f8f6f4 v[70:73], v[202:205], v[2:7], v[70:73], v240, v171 op_sel:[0,1,0] op_sel_hi:[0,0,0] cbsz:4 blgp:2
	v_mfma_scale_f32_16x16x128_f8f6f4 v[54:57], v[206:209], v[2:7], v[54:57], v240, v171 op_sel:[0,1,0] op_sel_hi:[0,0,0] cbsz:4 blgp:2
	v_mfma_scale_f32_16x16x128_f8f6f4 v[38:41], v[210:213], v[2:7], v[38:41], v240, v171 op_sel:[0,1,0] op_sel_hi:[0,0,0] cbsz:4 blgp:2
	v_mfma_scale_f32_16x16x128_f8f6f4 v[118:121], v[154:157], v[8:13], v[118:121], v240, v215 op_sel:[0,1,0] op_sel_hi:[0,0,0] cbsz:4 blgp:2
	v_mfma_scale_f32_16x16x128_f8f6f4 v[110:113], v[186:189], v[8:13], v[110:113], v240, v215 op_sel:[0,1,0] op_sel_hi:[0,0,0] cbsz:4 blgp:2
	v_mfma_scale_f32_16x16x128_f8f6f4 v[98:101], v[190:193], v[8:13], v[98:101], v240, v215 op_sel:[0,1,0] op_sel_hi:[0,0,0] cbsz:4 blgp:2
	v_mfma_scale_f32_16x16x128_f8f6f4 v[82:85], v[194:197], v[8:13], v[82:85], v240, v215 op_sel:[0,1,0] op_sel_hi:[0,0,0] cbsz:4 blgp:2
	v_mfma_scale_f32_16x16x128_f8f6f4 v[66:69], v[198:201], v[8:13], v[66:69], v240, v215 op_sel:[0,1,0] op_sel_hi:[0,0,0] cbsz:4 blgp:2
	v_mfma_scale_f32_16x16x128_f8f6f4 v[50:53], v[202:205], v[8:13], v[50:53], v240, v215 op_sel:[0,1,0] op_sel_hi:[0,0,0] cbsz:4 blgp:2
	v_mfma_scale_f32_16x16x128_f8f6f4 v[34:37], v[206:209], v[8:13], v[34:37], v240, v215 op_sel:[0,1,0] op_sel_hi:[0,0,0] cbsz:4 blgp:2
	v_mfma_scale_f32_16x16x128_f8f6f4 v[130:133], v[210:213], v[8:13], v[138:141], v240, v215 op_sel:[0,1,0] op_sel_hi:[0,0,0] cbsz:4 blgp:2
	v_mfma_scale_f32_16x16x128_f8f6f4 v[106:109], v[154:157], v[14:19], v[106:109], v240, v216 op_sel:[0,1,0] op_sel_hi:[0,0,0] cbsz:4 blgp:2
	v_mfma_scale_f32_16x16x128_f8f6f4 v[94:97], v[186:189], v[14:19], v[94:97], v240, v216 op_sel:[0,1,0] op_sel_hi:[0,0,0] cbsz:4 blgp:2
	v_mfma_scale_f32_16x16x128_f8f6f4 v[78:81], v[190:193], v[14:19], v[78:81], v240, v216 op_sel:[0,1,0] op_sel_hi:[0,0,0] cbsz:4 blgp:2
	v_mfma_scale_f32_16x16x128_f8f6f4 v[62:65], v[194:197], v[14:19], v[62:65], v240, v216 op_sel:[0,1,0] op_sel_hi:[0,0,0] cbsz:4 blgp:2
	v_mfma_scale_f32_16x16x128_f8f6f4 v[46:49], v[198:201], v[14:19], v[46:49], v240, v216 op_sel:[0,1,0] op_sel_hi:[0,0,0] cbsz:4 blgp:2
	v_mfma_scale_f32_16x16x128_f8f6f4 v[30:33], v[202:205], v[14:19], v[30:33], v240, v216 op_sel:[0,1,0] op_sel_hi:[0,0,0] cbsz:4 blgp:2
	v_mfma_scale_f32_16x16x128_f8f6f4 v[134:137], v[206:209], v[14:19], v[142:145], v240, v216 op_sel:[0,1,0] op_sel_hi:[0,0,0] cbsz:4 blgp:2
	v_mfma_scale_f32_16x16x128_f8f6f4 v[138:141], v[210:213], v[14:19], v[146:149], v240, v216 op_sel:[0,1,0] op_sel_hi:[0,0,0] cbsz:4 blgp:2
	v_mfma_scale_f32_16x16x128_f8f6f4 v[90:93], v[154:157], v[20:25], v[90:93], v240, v214 op_sel:[0,1,0] op_sel_hi:[0,0,0] cbsz:4 blgp:2
	v_mfma_scale_f32_16x16x128_f8f6f4 v[74:77], v[186:189], v[20:25], v[74:77], v240, v214 op_sel:[0,1,0] op_sel_hi:[0,0,0] cbsz:4 blgp:2
	v_mfma_scale_f32_16x16x128_f8f6f4 v[58:61], v[190:193], v[20:25], v[58:61], v240, v214 op_sel:[0,1,0] op_sel_hi:[0,0,0] cbsz:4 blgp:2
	v_mfma_scale_f32_16x16x128_f8f6f4 v[26:29], v[198:201], v[20:25], v[26:29], v240, v214 op_sel:[0,1,0] op_sel_hi:[0,0,0] cbsz:4 blgp:2
	v_mfma_scale_f32_16x16x128_f8f6f4 v[142:145], v[202:205], v[20:25], v[150:153], v240, v214 op_sel:[0,1,0] op_sel_hi:[0,0,0] cbsz:4 blgp:2
	v_mfma_scale_f32_16x16x128_f8f6f4 v[42:45], v[194:197], v[20:25], v[42:45], v240, v214 op_sel:[0,1,0] op_sel_hi:[0,0,0] cbsz:4 blgp:2
	v_mfma_scale_f32_16x16x128_f8f6f4 v[146:149], v[206:209], v[20:25], v[172:175], v240, v214 op_sel:[0,1,0] op_sel_hi:[0,0,0] cbsz:4 blgp:2
	v_mfma_scale_f32_16x16x128_f8f6f4 v[150:153], v[210:213], v[20:25], v[176:179], v240, v214 op_sel:[0,1,0] op_sel_hi:[0,0,0] cbsz:4 blgp:2
	s_barrier
	ds_read_b128 v[154:157], v166
	ds_read_b128 v[168:171], v166 offset:256
	ds_read_b128 v[172:175], v166 offset:512
	ds_read_b128 v[176:179], v166 offset:768
	ds_read_b128 v[180:183], v166 offset:1024
	ds_read_b128 v[184:187], v166 offset:1280
	ds_read_b128 v[188:191], v166 offset:1536
	ds_read_b128 v[192:195], v166 offset:1792
	ds_read_b64 v[2:3], v162
	ds_read_b64 v[4:5], v162 offset:8
	ds_read_b64 v[6:7], v162 offset:16
	ds_read_b64 v[8:9], v165
	ds_read_b64 v[10:11], v165 offset:8
	ds_read_b64 v[12:13], v165 offset:16
	ds_read_b64 v[14:15], v164
	ds_read_b64 v[16:17], v164 offset:8
	ds_read_b64 v[18:19], v164 offset:16
	ds_read_b64 v[20:21], v163
	ds_read_b64 v[22:23], v163 offset:8
	ds_read_b64 v[24:25], v163 offset:16
	v_add_u32_e32 v162, 0x21800, v161
	v_add_u32_e32 v163, 0x21820, v161
	v_add_u32_e32 v164, 0x21840, v161
	v_add_u32_e32 v161, 0x21860, v161
	ds_read_u16 v166, v162
	ds_read_u16 v167, v163
	ds_read_u16 v241, v164
	ds_read_u16 v161, v161
	s_waitcnt vmcnt(0)
	s_waitcnt lgkmcnt(0)
	s_waitcnt lgkmcnt(0)
	v_mov_b32_e32 v162, v166
	v_mov_b32_e32 v200, v167
	v_mov_b32_e32 v216, v241
	v_mov_b32_e32 v242, v161
	s_barrier
	v_mfma_scale_f32_16x16x128_f8f6f4 v[126:129], v[154:157], v[2:7], v[126:129], v240, v162 op_sel_hi:[0,0,0] cbsz:4 blgp:2
	v_mfma_scale_f32_16x16x128_f8f6f4 v[122:125], v[168:171], v[2:7], v[122:125], v240, v162 op_sel_hi:[0,0,0] cbsz:4 blgp:2
	v_mfma_scale_f32_16x16x128_f8f6f4 v[114:117], v[172:175], v[2:7], v[114:117], v240, v162 op_sel_hi:[0,0,0] cbsz:4 blgp:2
	v_mfma_scale_f32_16x16x128_f8f6f4 v[102:105], v[176:179], v[2:7], v[102:105], v240, v162 op_sel_hi:[0,0,0] cbsz:4 blgp:2
	v_mfma_scale_f32_16x16x128_f8f6f4 v[86:89], v[180:183], v[2:7], v[86:89], v240, v162 op_sel_hi:[0,0,0] cbsz:4 blgp:2
	v_mfma_scale_f32_16x16x128_f8f6f4 v[70:73], v[184:187], v[2:7], v[70:73], v240, v162 op_sel_hi:[0,0,0] cbsz:4 blgp:2
	v_mfma_scale_f32_16x16x128_f8f6f4 v[54:57], v[188:191], v[2:7], v[54:57], v240, v162 op_sel_hi:[0,0,0] cbsz:4 blgp:2
	v_mfma_scale_f32_16x16x128_f8f6f4 v[2:5], v[192:195], v[2:7], v[38:41], v240, v162 op_sel_hi:[0,0,0] cbsz:4 blgp:2
	v_mfma_scale_f32_16x16x128_f8f6f4 v[118:121], v[154:157], v[8:13], v[118:121], v240, v200 op_sel_hi:[0,0,0] cbsz:4 blgp:2
	v_mfma_scale_f32_16x16x128_f8f6f4 v[110:113], v[168:171], v[8:13], v[110:113], v240, v200 op_sel_hi:[0,0,0] cbsz:4 blgp:2
	v_mfma_scale_f32_16x16x128_f8f6f4 v[98:101], v[172:175], v[8:13], v[98:101], v240, v200 op_sel_hi:[0,0,0] cbsz:4 blgp:2
	v_mfma_scale_f32_16x16x128_f8f6f4 v[82:85], v[176:179], v[8:13], v[82:85], v240, v200 op_sel_hi:[0,0,0] cbsz:4 blgp:2
	v_mfma_scale_f32_16x16x128_f8f6f4 v[66:69], v[180:183], v[8:13], v[66:69], v240, v200 op_sel_hi:[0,0,0] cbsz:4 blgp:2
	v_mfma_scale_f32_16x16x128_f8f6f4 v[106:109], v[154:157], v[14:19], v[106:109], v240, v216 op_sel_hi:[0,0,0] cbsz:4 blgp:2
	v_mfma_scale_f32_16x16x128_f8f6f4 v[94:97], v[168:171], v[14:19], v[94:97], v240, v216 op_sel_hi:[0,0,0] cbsz:4 blgp:2
	v_mfma_scale_f32_16x16x128_f8f6f4 v[78:81], v[172:175], v[14:19], v[78:81], v240, v216 op_sel_hi:[0,0,0] cbsz:4 blgp:2
	v_mfma_scale_f32_16x16x128_f8f6f4 v[62:65], v[176:179], v[14:19], v[62:65], v240, v216 op_sel_hi:[0,0,0] cbsz:4 blgp:2
	v_mfma_scale_f32_16x16x128_f8f6f4 v[74:77], v[168:171], v[20:25], v[74:77], v240, v242 op_sel_hi:[0,0,0] cbsz:4 blgp:2
	v_mfma_scale_f32_16x16x128_f8f6f4 v[58:61], v[172:175], v[20:25], v[58:61], v240, v242 op_sel_hi:[0,0,0] cbsz:4 blgp:2
	v_mfma_scale_f32_16x16x128_f8f6f4 v[162:165], v[184:187], v[8:13], v[50:53], v240, v200 op_sel_hi:[0,0,0] cbsz:4 blgp:2
	v_mfma_scale_f32_16x16x128_f8f6f4 v[196:199], v[188:191], v[8:13], v[34:37], v240, v200 op_sel_hi:[0,0,0] cbsz:4 blgp:2
	v_mfma_scale_f32_16x16x128_f8f6f4 v[200:203], v[192:195], v[8:13], v[130:133], v240, v200 op_sel_hi:[0,0,0] cbsz:4 blgp:2
	v_mfma_scale_f32_16x16x128_f8f6f4 v[204:207], v[180:183], v[14:19], v[46:49], v240, v216 op_sel_hi:[0,0,0] cbsz:4 blgp:2
	v_mfma_scale_f32_16x16x128_f8f6f4 v[208:211], v[184:187], v[14:19], v[30:33], v240, v216 op_sel_hi:[0,0,0] cbsz:4 blgp:2
	v_mfma_scale_f32_16x16x128_f8f6f4 v[212:215], v[188:191], v[14:19], v[134:137], v240, v216 op_sel_hi:[0,0,0] cbsz:4 blgp:2
	v_mfma_scale_f32_16x16x128_f8f6f4 v[216:219], v[192:195], v[14:19], v[138:141], v240, v216 op_sel_hi:[0,0,0] cbsz:4 blgp:2
	v_mfma_scale_f32_16x16x128_f8f6f4 v[220:223], v[154:157], v[20:25], v[90:93], v240, v242 op_sel_hi:[0,0,0] cbsz:4 blgp:2
	v_mfma_scale_f32_16x16x128_f8f6f4 v[224:227], v[176:179], v[20:25], v[42:45], v240, v242 op_sel_hi:[0,0,0] cbsz:4 blgp:2
	v_mfma_scale_f32_16x16x128_f8f6f4 v[228:231], v[180:183], v[20:25], v[26:29], v240, v242 op_sel_hi:[0,0,0] cbsz:4 blgp:2
	v_mfma_scale_f32_16x16x128_f8f6f4 v[232:235], v[184:187], v[20:25], v[142:145], v240, v242 op_sel_hi:[0,0,0] cbsz:4 blgp:2
	v_mfma_scale_f32_16x16x128_f8f6f4 v[236:239], v[188:191], v[20:25], v[146:149], v240, v242 op_sel_hi:[0,0,0] cbsz:4 blgp:2
	v_mfma_scale_f32_16x16x128_f8f6f4 v[150:153], v[192:195], v[20:25], v[150:153], v240, v242 op_sel_hi:[0,0,0] cbsz:4 blgp:2
	s_barrier
	ds_read_b64 v[34:35], v1
	ds_read_b64 v[36:37], v1 offset:8
	ds_read_b64 v[38:39], v1 offset:16
	ds_read_b64 v[40:41], v160
	ds_read_b64 v[42:43], v160 offset:8
	ds_read_b64 v[44:45], v160 offset:16
	ds_read_b64 v[46:47], v159
	ds_read_b64 v[48:49], v159 offset:8
	ds_read_b64 v[50:51], v159 offset:16
	ds_read_b64 v[144:145], v158
	ds_read_b64 v[146:147], v158 offset:8
	ds_read_b64 v[148:149], v158 offset:16
	s_waitcnt lgkmcnt(0)
	v_lshrrev_b32_e32 v1, 8, v166
	v_lshrrev_b32_e32 v52, 8, v167
	v_lshrrev_b32_e32 v53, 8, v241
	v_lshrrev_b32_e32 v158, 8, v161
	s_barrier
	v_mfma_scale_f32_16x16x128_f8f6f4 v[30:33], v[154:157], v[34:39], v[126:129], v240, v1 op_sel_hi:[0,0,0] cbsz:4 blgp:2
	v_mfma_scale_f32_16x16x128_f8f6f4 v[22:25], v[168:171], v[34:39], v[122:125], v240, v1 op_sel_hi:[0,0,0] cbsz:4 blgp:2
	v_mfma_scale_f32_16x16x128_f8f6f4 v[14:17], v[172:175], v[34:39], v[114:117], v240, v1 op_sel_hi:[0,0,0] cbsz:4 blgp:2
	v_mfma_scale_f32_16x16x128_f8f6f4 v[6:9], v[176:179], v[34:39], v[102:105], v240, v1 op_sel_hi:[0,0,0] cbsz:4 blgp:2
	v_mfma_scale_f32_16x16x128_f8f6f4 v[26:29], v[180:183], v[34:39], v[86:89], v240, v1 op_sel_hi:[0,0,0] cbsz:4 blgp:2
	v_mfma_scale_f32_16x16x128_f8f6f4 v[18:21], v[184:187], v[34:39], v[70:73], v240, v1 op_sel_hi:[0,0,0] cbsz:4 blgp:2
	v_mfma_scale_f32_16x16x128_f8f6f4 v[10:13], v[188:191], v[34:39], v[54:57], v240, v1 op_sel_hi:[0,0,0] cbsz:4 blgp:2
	v_mfma_scale_f32_16x16x128_f8f6f4 v[2:5], v[192:195], v[34:39], v[2:5], v240, v1 op_sel_hi:[0,0,0] cbsz:4 blgp:2
	v_mfma_scale_f32_16x16x128_f8f6f4 v[132:135], v[154:157], v[40:45], v[118:121], v240, v52 op_sel_hi:[0,0,0] cbsz:4 blgp:2
	v_mfma_scale_f32_16x16x128_f8f6f4 v[128:131], v[168:171], v[40:45], v[110:113], v240, v52 op_sel_hi:[0,0,0] cbsz:4 blgp:2
	v_mfma_scale_f32_16x16x128_f8f6f4 v[124:127], v[172:175], v[40:45], v[98:101], v240, v52 op_sel_hi:[0,0,0] cbsz:4 blgp:2
	v_mfma_scale_f32_16x16x128_f8f6f4 v[116:119], v[176:179], v[40:45], v[82:85], v240, v52 op_sel_hi:[0,0,0] cbsz:4 blgp:2
	v_mfma_scale_f32_16x16x128_f8f6f4 v[140:143], v[180:183], v[40:45], v[66:69], v240, v52 op_sel_hi:[0,0,0] cbsz:4 blgp:2
	v_mfma_scale_f32_16x16x128_f8f6f4 v[136:139], v[184:187], v[40:45], v[162:165], v240, v52 op_sel_hi:[0,0,0] cbsz:4 blgp:2
	v_mfma_scale_f32_16x16x128_f8f6f4 v[120:123], v[188:191], v[40:45], v[196:199], v240, v52 op_sel_hi:[0,0,0] cbsz:4 blgp:2
	v_mfma_scale_f32_16x16x128_f8f6f4 v[112:115], v[192:195], v[40:45], v[200:203], v240, v52 op_sel_hi:[0,0,0] cbsz:4 blgp:2
	v_mfma_scale_f32_16x16x128_f8f6f4 v[100:103], v[154:157], v[46:51], v[106:109], v240, v53 op_sel_hi:[0,0,0] cbsz:4 blgp:2
	v_mfma_scale_f32_16x16x128_f8f6f4 v[96:99], v[168:171], v[46:51], v[94:97], v240, v53 op_sel_hi:[0,0,0] cbsz:4 blgp:2
	v_mfma_scale_f32_16x16x128_f8f6f4 v[92:95], v[172:175], v[46:51], v[78:81], v240, v53 op_sel_hi:[0,0,0] cbsz:4 blgp:2
	v_mfma_scale_f32_16x16x128_f8f6f4 v[84:87], v[176:179], v[46:51], v[62:65], v240, v53 op_sel_hi:[0,0,0] cbsz:4 blgp:2
	v_mfma_scale_f32_16x16x128_f8f6f4 v[108:111], v[180:183], v[46:51], v[204:207], v240, v53 op_sel_hi:[0,0,0] cbsz:4 blgp:2
	v_mfma_scale_f32_16x16x128_f8f6f4 v[104:107], v[184:187], v[46:51], v[208:211], v240, v53 op_sel_hi:[0,0,0] cbsz:4 blgp:2
	v_mfma_scale_f32_16x16x128_f8f6f4 v[88:91], v[188:191], v[46:51], v[212:215], v240, v53 op_sel_hi:[0,0,0] cbsz:4 blgp:2
	v_mfma_scale_f32_16x16x128_f8f6f4 v[80:83], v[192:195], v[46:51], v[216:219], v240, v53 op_sel_hi:[0,0,0] cbsz:4 blgp:2
	v_mfma_scale_f32_16x16x128_f8f6f4 v[68:71], v[154:157], v[144:149], v[220:223], v240, v158 op_sel_hi:[0,0,0] cbsz:4 blgp:2
	v_mfma_scale_f32_16x16x128_f8f6f4 v[64:67], v[168:171], v[144:149], v[74:77], v240, v158 op_sel_hi:[0,0,0] cbsz:4 blgp:2
	v_mfma_scale_f32_16x16x128_f8f6f4 v[60:63], v[172:175], v[144:149], v[58:61], v240, v158 op_sel_hi:[0,0,0] cbsz:4 blgp:2
	v_mfma_scale_f32_16x16x128_f8f6f4 v[52:55], v[176:179], v[144:149], v[224:227], v240, v158 op_sel_hi:[0,0,0] cbsz:4 blgp:2
	v_mfma_scale_f32_16x16x128_f8f6f4 v[76:79], v[180:183], v[144:149], v[228:231], v240, v158 op_sel_hi:[0,0,0] cbsz:4 blgp:2
	v_mfma_scale_f32_16x16x128_f8f6f4 v[72:75], v[184:187], v[144:149], v[232:235], v240, v158 op_sel_hi:[0,0,0] cbsz:4 blgp:2
	v_mfma_scale_f32_16x16x128_f8f6f4 v[56:59], v[188:191], v[144:149], v[236:239], v240, v158 op_sel_hi:[0,0,0] cbsz:4 blgp:2
	v_mfma_scale_f32_16x16x128_f8f6f4 v[48:51], v[192:195], v[144:149], v[150:153], v240, v158 op_sel_hi:[0,0,0] cbsz:4 blgp:2
	s_barrier
	s_cmpk_gt_u32 s33, 0xff
	s_cbranch_scc1 .LBB2_6
	s_barrier

.LBB3_3:
	s_add_i32 s42, s60, 0xfffff000
	s_and_b32 s42, s42, 0x1000
	ds_read_b128 v[202:205], v175
	ds_read_b128 v[206:209], v175 offset:256
	ds_read_b128 v[210:213], v175 offset:512
	ds_read_b128 v[214:217], v175 offset:768
	ds_read_b128 v[218:221], v175 offset:1024
	ds_read_b128 v[222:225], v175 offset:1280
	ds_read_b128 v[226:229], v175 offset:1536
	ds_read_b128 v[230:233], v175 offset:1792
	ds_read2_b64 v[178:181], v171 offset1:1
	ds_read2_b64 v[182:185], v171 offset0:2 offset1:48
	ds_read2_b64 v[186:189], v171 offset0:49 offset1:50
	s_mov_b32 m0, s57
	ds_read2_b64 v[190:193], v171 offset0:96 offset1:97
	global_load_lds_dwordx4 v144, s[76:77]
	s_mov_b32 m0, s56
	ds_read2_b64 v[194:197], v171 offset0:98 offset1:144
	global_load_lds_dwordx4 v145, s[76:77]
	s_mov_b32 m0, s55
	ds_read2_b64 v[198:201], v171 offset0:145 offset1:146
	global_load_lds_dwordx4 v146, s[76:77]
	v_add_u32_e32 v152, s42, v176
	ds_read_u16 v240, v152
	ds_read_u16 v241, v152 offset:32
	ds_read_u16 v242, v152 offset:64
	s_add_i32 s42, s60, 0xfffff800
	s_and_b32 s42, s42, 0x1800
	s_add_i32 m0, s48, s42
	ds_read_u16 v243, v152 offset:96
	global_load_lds_dword v150, s[80:81]
	s_waitcnt vmcnt(6)
	s_waitcnt lgkmcnt(0)
	s_barrier
	v_mfma_scale_f32_16x16x128_f8f6f4 v[126:129], v[202:205], v[178:183], v[126:129], v177, v240 op_sel_hi:[0,0,0] cbsz:4 blgp:2
	v_mfma_scale_f32_16x16x128_f8f6f4 v[122:125], v[206:209], v[178:183], v[122:125], v177, v240 op_sel_hi:[0,0,0] cbsz:4 blgp:2
	v_mfma_scale_f32_16x16x128_f8f6f4 v[114:117], v[210:213], v[178:183], v[114:117], v177, v240 op_sel_hi:[0,0,0] cbsz:4 blgp:2
	v_mfma_scale_f32_16x16x128_f8f6f4 v[102:105], v[214:217], v[178:183], v[102:105], v177, v240 op_sel_hi:[0,0,0] cbsz:4 blgp:2
	v_mfma_scale_f32_16x16x128_f8f6f4 v[86:89], v[218:221], v[178:183], v[86:89], v177, v240 op_sel_hi:[0,0,0] cbsz:4 blgp:2
	v_mfma_scale_f32_16x16x128_f8f6f4 v[70:73], v[222:225], v[178:183], v[70:73], v177, v240 op_sel_hi:[0,0,0] cbsz:4 blgp:2
	v_mfma_scale_f32_16x16x128_f8f6f4 v[54:57], v[226:229], v[178:183], v[54:57], v177, v240 op_sel_hi:[0,0,0] cbsz:4 blgp:2
	v_mfma_scale_f32_16x16x128_f8f6f4 v[38:41], v[230:233], v[178:183], v[38:41], v177, v240 op_sel_hi:[0,0,0] cbsz:4 blgp:2
	v_mfma_scale_f32_16x16x128_f8f6f4 v[118:121], v[202:205], v[184:189], v[118:121], v177, v241 op_sel_hi:[0,0,0] cbsz:4 blgp:2
	v_mfma_scale_f32_16x16x128_f8f6f4 v[110:113], v[206:209], v[184:189], v[110:113], v177, v241 op_sel_hi:[0,0,0] cbsz:4 blgp:2
	v_mfma_scale_f32_16x16x128_f8f6f4 v[98:101], v[210:213], v[184:189], v[98:101], v177, v241 op_sel_hi:[0,0,0] cbsz:4 blgp:2
	v_mfma_scale_f32_16x16x128_f8f6f4 v[82:85], v[214:217], v[184:189], v[82:85], v177, v241 op_sel_hi:[0,0,0] cbsz:4 blgp:2
	v_mfma_scale_f32_16x16x128_f8f6f4 v[66:69], v[218:221], v[184:189], v[66:69], v177, v241 op_sel_hi:[0,0,0] cbsz:4 blgp:2
	v_mfma_scale_f32_16x16x128_f8f6f4 v[50:53], v[222:225], v[184:189], v[50:53], v177, v241 op_sel_hi:[0,0,0] cbsz:4 blgp:2
	v_mfma_scale_f32_16x16x128_f8f6f4 v[34:37], v[226:229], v[184:189], v[34:37], v177, v241 op_sel_hi:[0,0,0] cbsz:4 blgp:2
	v_mfma_scale_f32_16x16x128_f8f6f4 v[106:109], v[202:205], v[190:195], v[106:109], v177, v242 op_sel_hi:[0,0,0] cbsz:4 blgp:2
	v_mfma_scale_f32_16x16x128_f8f6f4 v[94:97], v[206:209], v[190:195], v[94:97], v177, v242 op_sel_hi:[0,0,0] cbsz:4 blgp:2
	v_mfma_scale_f32_16x16x128_f8f6f4 v[78:81], v[210:213], v[190:195], v[78:81], v177, v242 op_sel_hi:[0,0,0] cbsz:4 blgp:2
	v_mfma_scale_f32_16x16x128_f8f6f4 v[62:65], v[214:217], v[190:195], v[62:65], v177, v242 op_sel_hi:[0,0,0] cbsz:4 blgp:2
	v_mfma_scale_f32_16x16x128_f8f6f4 v[46:49], v[218:221], v[190:195], v[46:49], v177, v242 op_sel_hi:[0,0,0] cbsz:4 blgp:2
	v_mfma_scale_f32_16x16x128_f8f6f4 v[30:33], v[222:225], v[190:195], v[30:33], v177, v242 op_sel_hi:[0,0,0] cbsz:4 blgp:2
	v_mfma_scale_f32_16x16x128_f8f6f4 v[90:93], v[202:205], v[196:201], v[90:93], v177, v243 op_sel_hi:[0,0,0] cbsz:4 blgp:2
	v_mfma_scale_f32_16x16x128_f8f6f4 v[74:77], v[206:209], v[196:201], v[74:77], v177, v243 op_sel_hi:[0,0,0] cbsz:4 blgp:2
	v_mfma_scale_f32_16x16x128_f8f6f4 v[58:61], v[210:213], v[196:201], v[58:61], v177, v243 op_sel_hi:[0,0,0] cbsz:4 blgp:2
	v_mfma_scale_f32_16x16x128_f8f6f4 v[42:45], v[214:217], v[196:201], v[42:45], v177, v243 op_sel_hi:[0,0,0] cbsz:4 blgp:2
	v_mfma_scale_f32_16x16x128_f8f6f4 v[26:29], v[218:221], v[196:201], v[26:29], v177, v243 op_sel_hi:[0,0,0] cbsz:4 blgp:2
	v_mfma_scale_f32_16x16x128_f8f6f4 v[178:181], v[230:233], v[184:189], v[22:25], v177, v241 op_sel_hi:[0,0,0] cbsz:4 blgp:2
	v_mfma_scale_f32_16x16x128_f8f6f4 v[182:185], v[226:229], v[190:195], v[18:21], v177, v242 op_sel_hi:[0,0,0] cbsz:4 blgp:2
	v_mfma_scale_f32_16x16x128_f8f6f4 v[186:189], v[230:233], v[190:195], v[10:13], v177, v242 op_sel_hi:[0,0,0] cbsz:4 blgp:2
	v_mfma_scale_f32_16x16x128_f8f6f4 v[190:193], v[222:225], v[196:201], v[14:17], v177, v243 op_sel_hi:[0,0,0] cbsz:4 blgp:2
	v_mfma_scale_f32_16x16x128_f8f6f4 v[234:237], v[226:229], v[196:201], v[6:9], v177, v243 op_sel_hi:[0,0,0] cbsz:4 blgp:2
	v_mfma_scale_f32_16x16x128_f8f6f4 v[194:197], v[230:233], v[196:201], v[2:5], v177, v243 op_sel_hi:[0,0,0] cbsz:4 blgp:2
	s_barrier
	ds_read2_b64 v[2:5], v167 offset1:1
	s_mov_b32 m0, s52
	ds_read2_b64 v[6:9], v167 offset0:2 offset1:48
	global_load_lds_dwordx4 v147, s[76:77]
	s_mov_b32 m0, s50
	ds_read2_b64 v[10:13], v167 offset0:49 offset1:50
	global_load_lds_dwordx4 v148, s[76:77]
	s_mov_b32 m0, s49
	ds_read2_b64 v[14:17], v167 offset0:96 offset1:97
	global_load_lds_dwordx4 v149, s[76:77]
	s_mov_b32 m0, s13
	ds_read2_b64 v[18:21], v167 offset0:98 offset1:144
	global_load_lds_dwordx4 v142, s[72:73]
	s_mov_b32 m0, s44
	ds_read2_b64 v[22:25], v167 offset0:145 offset1:146
	global_load_lds_dwordx4 v143, s[72:73]
	s_waitcnt vmcnt(5)
	s_waitcnt lgkmcnt(0)
	s_barrier
	v_mfma_scale_f32_16x16x128_f8f6f4 v[126:129], v[202:205], v[2:7], v[126:129], v177, v240 op_sel:[0,1,0] op_sel_hi:[0,0,0] cbsz:4 blgp:2
	v_mfma_scale_f32_16x16x128_f8f6f4 v[122:125], v[206:209], v[2:7], v[122:125], v177, v240 op_sel:[0,1,0] op_sel_hi:[0,0,0] cbsz:4 blgp:2
	v_mfma_scale_f32_16x16x128_f8f6f4 v[114:117], v[210:213], v[2:7], v[114:117], v177, v240 op_sel:[0,1,0] op_sel_hi:[0,0,0] cbsz:4 blgp:2
	v_mfma_scale_f32_16x16x128_f8f6f4 v[102:105], v[214:217], v[2:7], v[102:105], v177, v240 op_sel:[0,1,0] op_sel_hi:[0,0,0] cbsz:4 blgp:2
	v_mfma_scale_f32_16x16x128_f8f6f4 v[86:89], v[218:221], v[2:7], v[86:89], v177, v240 op_sel:[0,1,0] op_sel_hi:[0,0,0] cbsz:4 blgp:2
	v_mfma_scale_f32_16x16x128_f8f6f4 v[70:73], v[222:225], v[2:7], v[70:73], v177, v240 op_sel:[0,1,0] op_sel_hi:[0,0,0] cbsz:4 blgp:2
	v_mfma_scale_f32_16x16x128_f8f6f4 v[54:57], v[226:229], v[2:7], v[54:57], v177, v240 op_sel:[0,1,0] op_sel_hi:[0,0,0] cbsz:4 blgp:2
	v_mfma_scale_f32_16x16x128_f8f6f4 v[38:41], v[230:233], v[2:7], v[38:41], v177, v240 op_sel:[0,1,0] op_sel_hi:[0,0,0] cbsz:4 blgp:2
	v_mfma_scale_f32_16x16x128_f8f6f4 v[118:121], v[202:205], v[8:13], v[118:121], v177, v241 op_sel:[0,1,0] op_sel_hi:[0,0,0] cbsz:4 blgp:2
	v_mfma_scale_f32_16x16x128_f8f6f4 v[110:113], v[206:209], v[8:13], v[110:113], v177, v241 op_sel:[0,1,0] op_sel_hi:[0,0,0] cbsz:4 blgp:2
	v_mfma_scale_f32_16x16x128_f8f6f4 v[98:101], v[210:213], v[8:13], v[98:101], v177, v241 op_sel:[0,1,0] op_sel_hi:[0,0,0] cbsz:4 blgp:2
	v_mfma_scale_f32_16x16x128_f8f6f4 v[82:85], v[214:217], v[8:13], v[82:85], v177, v241 op_sel:[0,1,0] op_sel_hi:[0,0,0] cbsz:4 blgp:2
	v_mfma_scale_f32_16x16x128_f8f6f4 v[66:69], v[218:221], v[8:13], v[66:69], v177, v241 op_sel:[0,1,0] op_sel_hi:[0,0,0] cbsz:4 blgp:2
	v_mfma_scale_f32_16x16x128_f8f6f4 v[50:53], v[222:225], v[8:13], v[50:53], v177, v241 op_sel:[0,1,0] op_sel_hi:[0,0,0] cbsz:4 blgp:2
	v_mfma_scale_f32_16x16x128_f8f6f4 v[34:37], v[226:229], v[8:13], v[34:37], v177, v241 op_sel:[0,1,0] op_sel_hi:[0,0,0] cbsz:4 blgp:2
	v_mfma_scale_f32_16x16x128_f8f6f4 v[106:109], v[202:205], v[14:19], v[106:109], v177, v242 op_sel:[0,1,0] op_sel_hi:[0,0,0] cbsz:4 blgp:2
	v_mfma_scale_f32_16x16x128_f8f6f4 v[94:97], v[206:209], v[14:19], v[94:97], v177, v242 op_sel:[0,1,0] op_sel_hi:[0,0,0] cbsz:4 blgp:2
	v_mfma_scale_f32_16x16x128_f8f6f4 v[78:81], v[210:213], v[14:19], v[78:81], v177, v242 op_sel:[0,1,0] op_sel_hi:[0,0,0] cbsz:4 blgp:2
	v_mfma_scale_f32_16x16x128_f8f6f4 v[62:65], v[214:217], v[14:19], v[62:65], v177, v242 op_sel:[0,1,0] op_sel_hi:[0,0,0] cbsz:4 blgp:2
	v_mfma_scale_f32_16x16x128_f8f6f4 v[46:49], v[218:221], v[14:19], v[46:49], v177, v242 op_sel:[0,1,0] op_sel_hi:[0,0,0] cbsz:4 blgp:2
	v_mfma_scale_f32_16x16x128_f8f6f4 v[30:33], v[222:225], v[14:19], v[30:33], v177, v242 op_sel:[0,1,0] op_sel_hi:[0,0,0] cbsz:4 blgp:2
	v_mfma_scale_f32_16x16x128_f8f6f4 v[90:93], v[202:205], v[20:25], v[90:93], v177, v243 op_sel:[0,1,0] op_sel_hi:[0,0,0] cbsz:4 blgp:2
	v_mfma_scale_f32_16x16x128_f8f6f4 v[74:77], v[206:209], v[20:25], v[74:77], v177, v243 op_sel:[0,1,0] op_sel_hi:[0,0,0] cbsz:4 blgp:2
	v_mfma_scale_f32_16x16x128_f8f6f4 v[58:61], v[210:213], v[20:25], v[58:61], v177, v243 op_sel:[0,1,0] op_sel_hi:[0,0,0] cbsz:4 blgp:2
	v_mfma_scale_f32_16x16x128_f8f6f4 v[42:45], v[214:217], v[20:25], v[42:45], v177, v243 op_sel:[0,1,0] op_sel_hi:[0,0,0] cbsz:4 blgp:2
	v_mfma_scale_f32_16x16x128_f8f6f4 v[26:29], v[218:221], v[20:25], v[26:29], v177, v243 op_sel:[0,1,0] op_sel_hi:[0,0,0] cbsz:4 blgp:2
	v_mfma_scale_f32_16x16x128_f8f6f4 v[178:181], v[230:233], v[8:13], v[178:181], v177, v241 op_sel:[0,1,0] op_sel_hi:[0,0,0] cbsz:4 blgp:2
	v_mfma_scale_f32_16x16x128_f8f6f4 v[182:185], v[226:229], v[14:19], v[182:185], v177, v242 op_sel:[0,1,0] op_sel_hi:[0,0,0] cbsz:4 blgp:2
	v_mfma_scale_f32_16x16x128_f8f6f4 v[186:189], v[230:233], v[14:19], v[186:189], v177, v242 op_sel:[0,1,0] op_sel_hi:[0,0,0] cbsz:4 blgp:2
	v_mfma_scale_f32_16x16x128_f8f6f4 v[190:193], v[222:225], v[20:25], v[190:193], v177, v243 op_sel:[0,1,0] op_sel_hi:[0,0,0] cbsz:4 blgp:2
	v_mfma_scale_f32_16x16x128_f8f6f4 v[198:201], v[226:229], v[20:25], v[234:237], v177, v243 op_sel:[0,1,0] op_sel_hi:[0,0,0] cbsz:4 blgp:2
	v_mfma_scale_f32_16x16x128_f8f6f4 v[194:197], v[230:233], v[20:25], v[194:197], v177, v243 op_sel:[0,1,0] op_sel_hi:[0,0,0] cbsz:4 blgp:2
	s_barrier
	ds_read_b128 v[202:205], v166
	ds_read_b128 v[206:209], v166 offset:256
	ds_read_b128 v[210:213], v166 offset:512
	ds_read_b128 v[214:217], v166 offset:768
	ds_read_b128 v[218:221], v166 offset:1024
	ds_read_b128 v[222:225], v166 offset:1280
	ds_read_b128 v[226:229], v166 offset:1536
	ds_read_b128 v[230:233], v166 offset:1792
	ds_read2_b64 v[2:5], v162 offset1:1
	ds_read2_b64 v[6:9], v162 offset0:2 offset1:48
	ds_read2_b64 v[10:13], v162 offset0:49 offset1:50
	s_mov_b32 m0, s45
	ds_read2_b64 v[14:17], v162 offset0:96 offset1:97
	global_load_lds_dwordx4 v144, s[78:79]
	s_mov_b32 m0, s46
	ds_read2_b64 v[18:21], v162 offset0:98 offset1:144
	global_load_lds_dwordx4 v145, s[78:79]
	s_mov_b32 m0, s47
	ds_read2_b64 v[22:25], v162 offset0:145 offset1:146
	global_load_lds_dwordx4 v146, s[78:79]
	v_add_u32_e32 v234, s42, v176
	ds_read_u16 v242, v234
	ds_read_u16 v243, v234 offset:32
	ds_read_u16 v244, v234 offset:64
	s_and_b32 s42, s60, 0x1000
	s_add_i32 m0, s48, s42
	ds_read_u16 v245, v234 offset:96
	global_load_lds_dword v151, s[80:81]
	s_waitcnt vmcnt(6)
	s_waitcnt lgkmcnt(0)
	s_barrier
	v_mfma_scale_f32_16x16x128_f8f6f4 v[126:129], v[202:205], v[2:7], v[126:129], v177, v242 op_sel_hi:[0,0,0] cbsz:4 blgp:2
	v_mfma_scale_f32_16x16x128_f8f6f4 v[122:125], v[206:209], v[2:7], v[122:125], v177, v242 op_sel_hi:[0,0,0] cbsz:4 blgp:2
	v_mfma_scale_f32_16x16x128_f8f6f4 v[114:117], v[210:213], v[2:7], v[114:117], v177, v242 op_sel_hi:[0,0,0] cbsz:4 blgp:2
	v_mfma_scale_f32_16x16x128_f8f6f4 v[102:105], v[214:217], v[2:7], v[102:105], v177, v242 op_sel_hi:[0,0,0] cbsz:4 blgp:2
	v_mfma_scale_f32_16x16x128_f8f6f4 v[86:89], v[218:221], v[2:7], v[86:89], v177, v242 op_sel_hi:[0,0,0] cbsz:4 blgp:2
	v_mfma_scale_f32_16x16x128_f8f6f4 v[70:73], v[222:225], v[2:7], v[70:73], v177, v242 op_sel_hi:[0,0,0] cbsz:4 blgp:2
	v_mfma_scale_f32_16x16x128_f8f6f4 v[54:57], v[226:229], v[2:7], v[54:57], v177, v242 op_sel_hi:[0,0,0] cbsz:4 blgp:2
	v_mfma_scale_f32_16x16x128_f8f6f4 v[38:41], v[230:233], v[2:7], v[38:41], v177, v242 op_sel_hi:[0,0,0] cbsz:4 blgp:2
	v_mfma_scale_f32_16x16x128_f8f6f4 v[118:121], v[202:205], v[8:13], v[118:121], v177, v243 op_sel_hi:[0,0,0] cbsz:4 blgp:2
	v_mfma_scale_f32_16x16x128_f8f6f4 v[110:113], v[206:209], v[8:13], v[110:113], v177, v243 op_sel_hi:[0,0,0] cbsz:4 blgp:2
	v_mfma_scale_f32_16x16x128_f8f6f4 v[98:101], v[210:213], v[8:13], v[98:101], v177, v243 op_sel_hi:[0,0,0] cbsz:4 blgp:2
	v_mfma_scale_f32_16x16x128_f8f6f4 v[82:85], v[214:217], v[8:13], v[82:85], v177, v243 op_sel_hi:[0,0,0] cbsz:4 blgp:2
	v_mfma_scale_f32_16x16x128_f8f6f4 v[66:69], v[218:221], v[8:13], v[66:69], v177, v243 op_sel_hi:[0,0,0] cbsz:4 blgp:2
	v_mfma_scale_f32_16x16x128_f8f6f4 v[50:53], v[222:225], v[8:13], v[50:53], v177, v243 op_sel_hi:[0,0,0] cbsz:4 blgp:2
	v_mfma_scale_f32_16x16x128_f8f6f4 v[34:37], v[226:229], v[8:13], v[34:37], v177, v243 op_sel_hi:[0,0,0] cbsz:4 blgp:2
	v_mfma_scale_f32_16x16x128_f8f6f4 v[106:109], v[202:205], v[14:19], v[106:109], v177, v244 op_sel_hi:[0,0,0] cbsz:4 blgp:2
	v_mfma_scale_f32_16x16x128_f8f6f4 v[94:97], v[206:209], v[14:19], v[94:97], v177, v244 op_sel_hi:[0,0,0] cbsz:4 blgp:2
	v_mfma_scale_f32_16x16x128_f8f6f4 v[78:81], v[210:213], v[14:19], v[78:81], v177, v244 op_sel_hi:[0,0,0] cbsz:4 blgp:2
	v_mfma_scale_f32_16x16x128_f8f6f4 v[62:65], v[214:217], v[14:19], v[62:65], v177, v244 op_sel_hi:[0,0,0] cbsz:4 blgp:2
	v_mfma_scale_f32_16x16x128_f8f6f4 v[46:49], v[218:221], v[14:19], v[46:49], v177, v244 op_sel_hi:[0,0,0] cbsz:4 blgp:2
	v_mfma_scale_f32_16x16x128_f8f6f4 v[30:33], v[222:225], v[14:19], v[30:33], v177, v244 op_sel_hi:[0,0,0] cbsz:4 blgp:2
	v_mfma_scale_f32_16x16x128_f8f6f4 v[238:241], v[226:229], v[14:19], v[182:185], v177, v244 op_sel_hi:[0,0,0] cbsz:4 blgp:2
	v_mfma_scale_f32_16x16x128_f8f6f4 v[14:17], v[230:233], v[14:19], v[186:189], v177, v244 op_sel_hi:[0,0,0] cbsz:4 blgp:2
	v_mfma_scale_f32_16x16x128_f8f6f4 v[90:93], v[202:205], v[20:25], v[90:93], v177, v245 op_sel_hi:[0,0,0] cbsz:4 blgp:2
	v_mfma_scale_f32_16x16x128_f8f6f4 v[74:77], v[206:209], v[20:25], v[74:77], v177, v245 op_sel_hi:[0,0,0] cbsz:4 blgp:2
	v_mfma_scale_f32_16x16x128_f8f6f4 v[58:61], v[210:213], v[20:25], v[58:61], v177, v245 op_sel_hi:[0,0,0] cbsz:4 blgp:2
	v_mfma_scale_f32_16x16x128_f8f6f4 v[42:45], v[214:217], v[20:25], v[42:45], v177, v245 op_sel_hi:[0,0,0] cbsz:4 blgp:2
	v_mfma_scale_f32_16x16x128_f8f6f4 v[26:29], v[218:221], v[20:25], v[26:29], v177, v245 op_sel_hi:[0,0,0] cbsz:4 blgp:2
	v_mfma_scale_f32_16x16x128_f8f6f4 v[234:237], v[230:233], v[8:13], v[178:181], v177, v243 op_sel_hi:[0,0,0] cbsz:4 blgp:2
	v_mfma_scale_f32_16x16x128_f8f6f4 v[190:193], v[222:225], v[20:25], v[190:193], v177, v245 op_sel_hi:[0,0,0] cbsz:4 blgp:2
	v_mfma_scale_f32_16x16x128_f8f6f4 v[198:201], v[226:229], v[20:25], v[198:201], v177, v245 op_sel_hi:[0,0,0] cbsz:4 blgp:2
	v_mfma_scale_f32_16x16x128_f8f6f4 v[194:197], v[230:233], v[20:25], v[194:197], v177, v245 op_sel_hi:[0,0,0] cbsz:4 blgp:2
	s_barrier
	ds_read2_b64 v[2:5], v1 offset1:1
	s_mov_b32 m0, s51
	ds_read2_b64 v[6:9], v1 offset0:2 offset1:48
	global_load_lds_dwordx4 v147, s[78:79]
	s_mov_b32 m0, s53
	ds_read2_b64 v[10:13], v1 offset0:49 offset1:50
	global_load_lds_dwordx4 v148, s[78:79]
	s_mov_b32 m0, s54
	ds_read2_b64 v[178:181], v159 offset1:1
	global_load_lds_dwordx4 v149, s[78:79]
	s_mov_b32 m0, s61
	ds_read2_b64 v[182:185], v159 offset0:2 offset1:48
	global_load_lds_dwordx4 v142, s[74:75]
	s_mov_b32 m0, s58
	ds_read2_b64 v[186:189], v159 offset0:49 offset1:50
	global_load_lds_dwordx4 v143, s[74:75]
	s_waitcnt vmcnt(5)
	s_waitcnt lgkmcnt(0)
	s_barrier
	v_mfma_scale_f32_16x16x128_f8f6f4 v[126:129], v[202:205], v[2:7], v[126:129], v177, v242 op_sel:[0,1,0] op_sel_hi:[0,0,0] cbsz:4 blgp:2
	v_mfma_scale_f32_16x16x128_f8f6f4 v[122:125], v[206:209], v[2:7], v[122:125], v177, v242 op_sel:[0,1,0] op_sel_hi:[0,0,0] cbsz:4 blgp:2
	v_mfma_scale_f32_16x16x128_f8f6f4 v[114:117], v[210:213], v[2:7], v[114:117], v177, v242 op_sel:[0,1,0] op_sel_hi:[0,0,0] cbsz:4 blgp:2
	v_mfma_scale_f32_16x16x128_f8f6f4 v[102:105], v[214:217], v[2:7], v[102:105], v177, v242 op_sel:[0,1,0] op_sel_hi:[0,0,0] cbsz:4 blgp:2
	v_mfma_scale_f32_16x16x128_f8f6f4 v[86:89], v[218:221], v[2:7], v[86:89], v177, v242 op_sel:[0,1,0] op_sel_hi:[0,0,0] cbsz:4 blgp:2
	v_mfma_scale_f32_16x16x128_f8f6f4 v[70:73], v[222:225], v[2:7], v[70:73], v177, v242 op_sel:[0,1,0] op_sel_hi:[0,0,0] cbsz:4 blgp:2
	v_mfma_scale_f32_16x16x128_f8f6f4 v[54:57], v[226:229], v[2:7], v[54:57], v177, v242 op_sel:[0,1,0] op_sel_hi:[0,0,0] cbsz:4 blgp:2
	v_mfma_scale_f32_16x16x128_f8f6f4 v[38:41], v[230:233], v[2:7], v[38:41], v177, v242 op_sel:[0,1,0] op_sel_hi:[0,0,0] cbsz:4 blgp:2
	v_mfma_scale_f32_16x16x128_f8f6f4 v[118:121], v[202:205], v[8:13], v[118:121], v177, v243 op_sel:[0,1,0] op_sel_hi:[0,0,0] cbsz:4 blgp:2
	v_mfma_scale_f32_16x16x128_f8f6f4 v[110:113], v[206:209], v[8:13], v[110:113], v177, v243 op_sel:[0,1,0] op_sel_hi:[0,0,0] cbsz:4 blgp:2
	v_mfma_scale_f32_16x16x128_f8f6f4 v[98:101], v[210:213], v[8:13], v[98:101], v177, v243 op_sel:[0,1,0] op_sel_hi:[0,0,0] cbsz:4 blgp:2
	v_mfma_scale_f32_16x16x128_f8f6f4 v[82:85], v[214:217], v[8:13], v[82:85], v177, v243 op_sel:[0,1,0] op_sel_hi:[0,0,0] cbsz:4 blgp:2
	v_mfma_scale_f32_16x16x128_f8f6f4 v[66:69], v[218:221], v[8:13], v[66:69], v177, v243 op_sel:[0,1,0] op_sel_hi:[0,0,0] cbsz:4 blgp:2
	v_mfma_scale_f32_16x16x128_f8f6f4 v[50:53], v[222:225], v[8:13], v[50:53], v177, v243 op_sel:[0,1,0] op_sel_hi:[0,0,0] cbsz:4 blgp:2
	v_mfma_scale_f32_16x16x128_f8f6f4 v[34:37], v[226:229], v[8:13], v[34:37], v177, v243 op_sel:[0,1,0] op_sel_hi:[0,0,0] cbsz:4 blgp:2
	v_mfma_scale_f32_16x16x128_f8f6f4 v[22:25], v[230:233], v[8:13], v[234:237], v177, v243 op_sel:[0,1,0] op_sel_hi:[0,0,0] cbsz:4 blgp:2
	v_mfma_scale_f32_16x16x128_f8f6f4 v[106:109], v[202:205], v[178:183], v[106:109], v177, v244 op_sel:[0,1,0] op_sel_hi:[0,0,0] cbsz:4 blgp:2
	v_mfma_scale_f32_16x16x128_f8f6f4 v[94:97], v[206:209], v[178:183], v[94:97], v177, v244 op_sel:[0,1,0] op_sel_hi:[0,0,0] cbsz:4 blgp:2
	v_mfma_scale_f32_16x16x128_f8f6f4 v[78:81], v[210:213], v[178:183], v[78:81], v177, v244 op_sel:[0,1,0] op_sel_hi:[0,0,0] cbsz:4 blgp:2
	v_mfma_scale_f32_16x16x128_f8f6f4 v[62:65], v[214:217], v[178:183], v[62:65], v177, v244 op_sel:[0,1,0] op_sel_hi:[0,0,0] cbsz:4 blgp:2
	v_mfma_scale_f32_16x16x128_f8f6f4 v[46:49], v[218:221], v[178:183], v[46:49], v177, v244 op_sel:[0,1,0] op_sel_hi:[0,0,0] cbsz:4 blgp:2
	v_mfma_scale_f32_16x16x128_f8f6f4 v[30:33], v[222:225], v[178:183], v[30:33], v177, v244 op_sel:[0,1,0] op_sel_hi:[0,0,0] cbsz:4 blgp:2
	v_mfma_scale_f32_16x16x128_f8f6f4 v[18:21], v[226:229], v[178:183], v[238:241], v177, v244 op_sel:[0,1,0] op_sel_hi:[0,0,0] cbsz:4 blgp:2
	v_mfma_scale_f32_16x16x128_f8f6f4 v[10:13], v[230:233], v[178:183], v[14:17], v177, v244 op_sel:[0,1,0] op_sel_hi:[0,0,0] cbsz:4 blgp:2
	v_mfma_scale_f32_16x16x128_f8f6f4 v[90:93], v[202:205], v[184:189], v[90:93], v177, v245 op_sel:[0,1,0] op_sel_hi:[0,0,0] cbsz:4 blgp:2
	v_mfma_scale_f32_16x16x128_f8f6f4 v[74:77], v[206:209], v[184:189], v[74:77], v177, v245 op_sel:[0,1,0] op_sel_hi:[0,0,0] cbsz:4 blgp:2
	v_mfma_scale_f32_16x16x128_f8f6f4 v[58:61], v[210:213], v[184:189], v[58:61], v177, v245 op_sel:[0,1,0] op_sel_hi:[0,0,0] cbsz:4 blgp:2
	v_mfma_scale_f32_16x16x128_f8f6f4 v[42:45], v[214:217], v[184:189], v[42:45], v177, v245 op_sel:[0,1,0] op_sel_hi:[0,0,0] cbsz:4 blgp:2
	v_mfma_scale_f32_16x16x128_f8f6f4 v[26:29], v[218:221], v[184:189], v[26:29], v177, v245 op_sel:[0,1,0] op_sel_hi:[0,0,0] cbsz:4 blgp:2
	v_mfma_scale_f32_16x16x128_f8f6f4 v[14:17], v[222:225], v[184:189], v[190:193], v177, v245 op_sel:[0,1,0] op_sel_hi:[0,0,0] cbsz:4 blgp:2
	v_mfma_scale_f32_16x16x128_f8f6f4 v[6:9], v[226:229], v[184:189], v[198:201], v177, v245 op_sel:[0,1,0] op_sel_hi:[0,0,0] cbsz:4 blgp:2
	v_mfma_scale_f32_16x16x128_f8f6f4 v[2:5], v[230:233], v[184:189], v[194:197], v177, v245 op_sel:[0,1,0] op_sel_hi:[0,0,0] cbsz:4 blgp:2
	s_barrier
	s_add_i32 s59, s59, 2
	s_addk_i32 s60, 0x1000
	s_add_u32 s72, s72, 0x8000
	s_addc_u32 s73, s73, 0
	s_add_u32 s74, s74, 0x8000
	s_addc_u32 s75, s75, 0
	s_add_u32 s76, s76, 0x18000
	s_addc_u32 s77, s77, 0
	s_add_u32 s78, s78, 0x18000
	s_addc_u32 s79, s79, 0
	s_add_u32 s80, s80, 0x1000
	s_addc_u32 s81, s81, 0
	s_cmp_lt_u32 s59, 28
	s_cbranch_scc1 .LBB3_3
	s_mov_b32 m0, s57
	s_nop 0
	global_load_lds_dwordx4 v144, s[76:77]
	s_mov_b32 m0, s56
	s_nop 0
	global_load_lds_dwordx4 v145, s[76:77]
	s_mov_b32 m0, s55
	s_nop 0
	global_load_lds_dwordx4 v146, s[76:77]
	s_add_i32 m0, s9, 0x21800
	s_nop 0
	global_load_lds_dword v150, s[80:81]
	s_mov_b32 m0, s52
	s_nop 0
	global_load_lds_dwordx4 v147, s[76:77]
	s_mov_b32 m0, s50
	s_nop 0
	global_load_lds_dwordx4 v148, s[76:77]
	s_mov_b32 m0, s49
	s_nop 0
	global_load_lds_dwordx4 v149, s[76:77]
	ds_read_b128 v[154:157], v175
	ds_read_b128 v[186:189], v175 offset:256
	ds_read_b128 v[190:193], v175 offset:512
	ds_read_b128 v[194:197], v175 offset:768
	ds_read_b128 v[198:201], v175 offset:1024
	ds_read_b128 v[202:205], v175 offset:1280
	ds_read_b128 v[206:209], v175 offset:1536
	ds_read_b128 v[210:213], v175 offset:1792
	ds_read_b64 v[142:143], v171
	ds_read_b64 v[144:145], v171 offset:8
	ds_read_b64 v[146:147], v171 offset:16
	ds_read_b64 v[148:149], v174
	ds_read_b64 v[150:151], v174 offset:8
	ds_read_b64 v[152:153], v174 offset:16
	ds_read_b64 v[174:175], v173
	ds_read_b64 v[176:177], v173 offset:8
	ds_read_b64 v[178:179], v173 offset:16
	ds_read_b64 v[180:181], v172
	ds_read_b64 v[182:183], v172 offset:8
	ds_read_b64 v[184:185], v172 offset:16
	v_add_u32_e32 v171, 0x21000, v248
	ds_read_u16 v215, v171 offset:32
	ds_read_u16 v216, v171 offset:64
	ds_read_u16 v214, v171 offset:96
	ds_read_u16 v171, v171
	s_waitcnt vmcnt(9)
	s_waitcnt lgkmcnt(0)
	s_barrier
	v_mov_b32_e32 v161, 0x7f7f7f7f
	s_nop 1
	v_mfma_scale_f32_16x16x128_f8f6f4 v[126:129], v[154:157], v[142:147], v[126:129], v161, v171 op_sel_hi:[0,0,0] cbsz:4 blgp:2
	v_mfma_scale_f32_16x16x128_f8f6f4 v[122:125], v[186:189], v[142:147], v[122:125], v161, v171 op_sel_hi:[0,0,0] cbsz:4 blgp:2
	v_mfma_scale_f32_16x16x128_f8f6f4 v[114:117], v[190:193], v[142:147], v[114:117], v161, v171 op_sel_hi:[0,0,0] cbsz:4 blgp:2
	v_mfma_scale_f32_16x16x128_f8f6f4 v[102:105], v[194:197], v[142:147], v[102:105], v161, v171 op_sel_hi:[0,0,0] cbsz:4 blgp:2
	v_mfma_scale_f32_16x16x128_f8f6f4 v[86:89], v[198:201], v[142:147], v[86:89], v161, v171 op_sel_hi:[0,0,0] cbsz:4 blgp:2
	v_mfma_scale_f32_16x16x128_f8f6f4 v[70:73], v[202:205], v[142:147], v[70:73], v161, v171 op_sel_hi:[0,0,0] cbsz:4 blgp:2
	v_mfma_scale_f32_16x16x128_f8f6f4 v[54:57], v[206:209], v[142:147], v[54:57], v161, v171 op_sel_hi:[0,0,0] cbsz:4 blgp:2
	v_mfma_scale_f32_16x16x128_f8f6f4 v[38:41], v[210:213], v[142:147], v[38:41], v161, v171 op_sel_hi:[0,0,0] cbsz:4 blgp:2
	v_mfma_scale_f32_16x16x128_f8f6f4 v[118:121], v[154:157], v[148:153], v[118:121], v161, v215 op_sel_hi:[0,0,0] cbsz:4 blgp:2
	v_mfma_scale_f32_16x16x128_f8f6f4 v[110:113], v[186:189], v[148:153], v[110:113], v161, v215 op_sel_hi:[0,0,0] cbsz:4 blgp:2
	v_mfma_scale_f32_16x16x128_f8f6f4 v[98:101], v[190:193], v[148:153], v[98:101], v161, v215 op_sel_hi:[0,0,0] cbsz:4 blgp:2
	v_mfma_scale_f32_16x16x128_f8f6f4 v[82:85], v[194:197], v[148:153], v[82:85], v161, v215 op_sel_hi:[0,0,0] cbsz:4 blgp:2
	v_mfma_scale_f32_16x16x128_f8f6f4 v[66:69], v[198:201], v[148:153], v[66:69], v161, v215 op_sel_hi:[0,0,0] cbsz:4 blgp:2
	v_mfma_scale_f32_16x16x128_f8f6f4 v[50:53], v[202:205], v[148:153], v[50:53], v161, v215 op_sel_hi:[0,0,0] cbsz:4 blgp:2
	v_mfma_scale_f32_16x16x128_f8f6f4 v[34:37], v[206:209], v[148:153], v[34:37], v161, v215 op_sel_hi:[0,0,0] cbsz:4 blgp:2
	v_mfma_scale_f32_16x16x128_f8f6f4 v[138:141], v[210:213], v[148:153], v[22:25], v161, v215 op_sel_hi:[0,0,0] cbsz:4 blgp:2
	v_mfma_scale_f32_16x16x128_f8f6f4 v[106:109], v[154:157], v[174:179], v[106:109], v161, v216 op_sel_hi:[0,0,0] cbsz:4 blgp:2
	v_mfma_scale_f32_16x16x128_f8f6f4 v[94:97], v[186:189], v[174:179], v[94:97], v161, v216 op_sel_hi:[0,0,0] cbsz:4 blgp:2
	v_mfma_scale_f32_16x16x128_f8f6f4 v[78:81], v[190:193], v[174:179], v[78:81], v161, v216 op_sel_hi:[0,0,0] cbsz:4 blgp:2
	v_mfma_scale_f32_16x16x128_f8f6f4 v[62:65], v[194:197], v[174:179], v[62:65], v161, v216 op_sel_hi:[0,0,0] cbsz:4 blgp:2
	v_mfma_scale_f32_16x16x128_f8f6f4 v[46:49], v[198:201], v[174:179], v[46:49], v161, v216 op_sel_hi:[0,0,0] cbsz:4 blgp:2
	v_mfma_scale_f32_16x16x128_f8f6f4 v[142:145], v[206:209], v[174:179], v[18:21], v161, v216 op_sel_hi:[0,0,0] cbsz:4 blgp:2
	v_mfma_scale_f32_16x16x128_f8f6f4 v[146:149], v[210:213], v[174:179], v[10:13], v161, v216 op_sel_hi:[0,0,0] cbsz:4 blgp:2
	v_mfma_scale_f32_16x16x128_f8f6f4 v[90:93], v[154:157], v[180:185], v[90:93], v161, v214 op_sel_hi:[0,0,0] cbsz:4 blgp:2
	v_mfma_scale_f32_16x16x128_f8f6f4 v[74:77], v[186:189], v[180:185], v[74:77], v161, v214 op_sel_hi:[0,0,0] cbsz:4 blgp:2
	v_mfma_scale_f32_16x16x128_f8f6f4 v[58:61], v[190:193], v[180:185], v[58:61], v161, v214 op_sel_hi:[0,0,0] cbsz:4 blgp:2
	v_mfma_scale_f32_16x16x128_f8f6f4 v[150:153], v[202:205], v[180:185], v[14:17], v161, v214 op_sel_hi:[0,0,0] cbsz:4 blgp:2
	v_mfma_scale_f32_16x16x128_f8f6f4 v[30:33], v[202:205], v[174:179], v[30:33], v161, v216 op_sel_hi:[0,0,0] cbsz:4 blgp:2
	v_mfma_scale_f32_16x16x128_f8f6f4 v[42:45], v[194:197], v[180:185], v[42:45], v161, v214 op_sel_hi:[0,0,0] cbsz:4 blgp:2
	v_mfma_scale_f32_16x16x128_f8f6f4 v[26:29], v[198:201], v[180:185], v[26:29], v161, v214 op_sel_hi:[0,0,0] cbsz:4 blgp:2
	v_mfma_scale_f32_16x16x128_f8f6f4 v[172:175], v[206:209], v[180:185], v[6:9], v161, v214 op_sel_hi:[0,0,0] cbsz:4 blgp:2
	v_mfma_scale_f32_16x16x128_f8f6f4 v[176:179], v[210:213], v[180:185], v[2:5], v161, v214 op_sel_hi:[0,0,0] cbsz:4 blgp:2
	s_barrier
	ds_read_b64 v[2:3], v167
	ds_read_b64 v[4:5], v167 offset:8
	ds_read_b64 v[6:7], v167 offset:16
	ds_read_b64 v[8:9], v170
	ds_read_b64 v[10:11], v170 offset:8
	ds_read_b64 v[12:13], v170 offset:16
	ds_read_b64 v[14:15], v169
	ds_read_b64 v[16:17], v169 offset:8
	ds_read_b64 v[18:19], v169 offset:16
	ds_read_b64 v[20:21], v168
	ds_read_b64 v[22:23], v168 offset:8
	ds_read_b64 v[24:25], v168 offset:16
	s_waitcnt vmcnt(3)
	s_waitcnt lgkmcnt(0)
	s_barrier
	v_mfma_scale_f32_16x16x128_f8f6f4 v[126:129], v[154:157], v[2:7], v[126:129], v161, v171 op_sel:[0,1,0] op_sel_hi:[0,0,0] cbsz:4 blgp:2
	v_mfma_scale_f32_16x16x128_f8f6f4 v[122:125], v[186:189], v[2:7], v[122:125], v161, v171 op_sel:[0,1,0] op_sel_hi:[0,0,0] cbsz:4 blgp:2
	v_mfma_scale_f32_16x16x128_f8f6f4 v[114:117], v[190:193], v[2:7], v[114:117], v161, v171 op_sel:[0,1,0] op_sel_hi:[0,0,0] cbsz:4 blgp:2
	v_mfma_scale_f32_16x16x128_f8f6f4 v[102:105], v[194:197], v[2:7], v[102:105], v161, v171 op_sel:[0,1,0] op_sel_hi:[0,0,0] cbsz:4 blgp:2
	v_mfma_scale_f32_16x16x128_f8f6f4 v[86:89], v[198:201], v[2:7], v[86:89], v161, v171 op_sel:[0,1,0] op_sel_hi:[0,0,0] cbsz:4 blgp:2
	v_mfma_scale_f32_16x16x128_f8f6f4 v[70:73], v[202:205], v[2:7], v[70:73], v161, v171 op_sel:[0,1,0] op_sel_hi:[0,0,0] cbsz:4 blgp:2
	v_mfma_scale_f32_16x16x128_f8f6f4 v[54:57], v[206:209], v[2:7], v[54:57], v161, v171 op_sel:[0,1,0] op_sel_hi:[0,0,0] cbsz:4 blgp:2
	v_mfma_scale_f32_16x16x128_f8f6f4 v[38:41], v[210:213], v[2:7], v[38:41], v161, v171 op_sel:[0,1,0] op_sel_hi:[0,0,0] cbsz:4 blgp:2
	v_mfma_scale_f32_16x16x128_f8f6f4 v[118:121], v[154:157], v[8:13], v[118:121], v161, v215 op_sel:[0,1,0] op_sel_hi:[0,0,0] cbsz:4 blgp:2
	v_mfma_scale_f32_16x16x128_f8f6f4 v[110:113], v[186:189], v[8:13], v[110:113], v161, v215 op_sel:[0,1,0] op_sel_hi:[0,0,0] cbsz:4 blgp:2
	v_mfma_scale_f32_16x16x128_f8f6f4 v[98:101], v[190:193], v[8:13], v[98:101], v161, v215 op_sel:[0,1,0] op_sel_hi:[0,0,0] cbsz:4 blgp:2
	v_mfma_scale_f32_16x16x128_f8f6f4 v[82:85], v[194:197], v[8:13], v[82:85], v161, v215 op_sel:[0,1,0] op_sel_hi:[0,0,0] cbsz:4 blgp:2
	v_mfma_scale_f32_16x16x128_f8f6f4 v[66:69], v[198:201], v[8:13], v[66:69], v161, v215 op_sel:[0,1,0] op_sel_hi:[0,0,0] cbsz:4 blgp:2
	v_mfma_scale_f32_16x16x128_f8f6f4 v[50:53], v[202:205], v[8:13], v[50:53], v161, v215 op_sel:[0,1,0] op_sel_hi:[0,0,0] cbsz:4 blgp:2
	v_mfma_scale_f32_16x16x128_f8f6f4 v[34:37], v[206:209], v[8:13], v[34:37], v161, v215 op_sel:[0,1,0] op_sel_hi:[0,0,0] cbsz:4 blgp:2
	v_mfma_scale_f32_16x16x128_f8f6f4 v[130:133], v[210:213], v[8:13], v[138:141], v161, v215 op_sel:[0,1,0] op_sel_hi:[0,0,0] cbsz:4 blgp:2
	v_mfma_scale_f32_16x16x128_f8f6f4 v[106:109], v[154:157], v[14:19], v[106:109], v161, v216 op_sel:[0,1,0] op_sel_hi:[0,0,0] cbsz:4 blgp:2
	v_mfma_scale_f32_16x16x128_f8f6f4 v[94:97], v[186:189], v[14:19], v[94:97], v161, v216 op_sel:[0,1,0] op_sel_hi:[0,0,0] cbsz:4 blgp:2
	v_mfma_scale_f32_16x16x128_f8f6f4 v[78:81], v[190:193], v[14:19], v[78:81], v161, v216 op_sel:[0,1,0] op_sel_hi:[0,0,0] cbsz:4 blgp:2
	v_mfma_scale_f32_16x16x128_f8f6f4 v[62:65], v[194:197], v[14:19], v[62:65], v161, v216 op_sel:[0,1,0] op_sel_hi:[0,0,0] cbsz:4 blgp:2
	v_mfma_scale_f32_16x16x128_f8f6f4 v[46:49], v[198:201], v[14:19], v[46:49], v161, v216 op_sel:[0,1,0] op_sel_hi:[0,0,0] cbsz:4 blgp:2
	v_mfma_scale_f32_16x16x128_f8f6f4 v[134:137], v[206:209], v[14:19], v[142:145], v161, v216 op_sel:[0,1,0] op_sel_hi:[0,0,0] cbsz:4 blgp:2
	v_mfma_scale_f32_16x16x128_f8f6f4 v[138:141], v[210:213], v[14:19], v[146:149], v161, v216 op_sel:[0,1,0] op_sel_hi:[0,0,0] cbsz:4 blgp:2
	v_mfma_scale_f32_16x16x128_f8f6f4 v[90:93], v[154:157], v[20:25], v[90:93], v161, v214 op_sel:[0,1,0] op_sel_hi:[0,0,0] cbsz:4 blgp:2
	v_mfma_scale_f32_16x16x128_f8f6f4 v[58:61], v[190:193], v[20:25], v[58:61], v161, v214 op_sel:[0,1,0] op_sel_hi:[0,0,0] cbsz:4 blgp:2
	v_mfma_scale_f32_16x16x128_f8f6f4 v[142:145], v[202:205], v[20:25], v[150:153], v161, v214 op_sel:[0,1,0] op_sel_hi:[0,0,0] cbsz:4 blgp:2
	v_mfma_scale_f32_16x16x128_f8f6f4 v[146:149], v[206:209], v[20:25], v[172:175], v161, v214 op_sel:[0,1,0] op_sel_hi:[0,0,0] cbsz:4 blgp:2
	v_mfma_scale_f32_16x16x128_f8f6f4 v[150:153], v[210:213], v[20:25], v[176:179], v161, v214 op_sel:[0,1,0] op_sel_hi:[0,0,0] cbsz:4 blgp:2
	v_mfma_scale_f32_16x16x128_f8f6f4 v[30:33], v[202:205], v[14:19], v[30:33], v161, v216 op_sel:[0,1,0] op_sel_hi:[0,0,0] cbsz:4 blgp:2
	v_mfma_scale_f32_16x16x128_f8f6f4 v[236:239], v[186:189], v[20:25], v[74:77], v161, v214 op_sel:[0,1,0] op_sel_hi:[0,0,0] cbsz:4 blgp:2
	v_mfma_scale_f32_16x16x128_f8f6f4 v[42:45], v[194:197], v[20:25], v[42:45], v161, v214 op_sel:[0,1,0] op_sel_hi:[0,0,0] cbsz:4 blgp:2
	v_mfma_scale_f32_16x16x128_f8f6f4 v[26:29], v[198:201], v[20:25], v[26:29], v161, v214 op_sel:[0,1,0] op_sel_hi:[0,0,0] cbsz:4 blgp:2
	s_barrier
	ds_read_b128 v[168:171], v166
	ds_read_b128 v[172:175], v166 offset:256
	ds_read_b128 v[176:179], v166 offset:512
	ds_read_b128 v[180:183], v166 offset:768
	ds_read_b128 v[184:187], v166 offset:1024
	ds_read_b128 v[188:191], v166 offset:1280
	ds_read_b128 v[192:195], v166 offset:1536
	ds_read_b128 v[196:199], v166 offset:1792
	ds_read_b64 v[2:3], v162
	ds_read_b64 v[4:5], v162 offset:8
	ds_read_b64 v[6:7], v162 offset:16
	ds_read_b64 v[8:9], v165
	ds_read_b64 v[10:11], v165 offset:8
	ds_read_b64 v[12:13], v165 offset:16
	ds_read_b64 v[14:15], v164
	ds_read_b64 v[16:17], v164 offset:8
	ds_read_b64 v[18:19], v164 offset:16
	ds_read_b64 v[20:21], v163
	ds_read_b64 v[22:23], v163 offset:8
	ds_read_b64 v[24:25], v163 offset:16
	v_add_u32_e32 v154, 0x21800, v248
	v_add_u32_e32 v155, 0x21820, v248
	v_add_u32_e32 v156, 0x21840, v248
	v_add_u32_e32 v157, 0x21860, v248
	ds_read_u16 v166, v154
	ds_read_u16 v167, v155
	ds_read_u16 v74, v156
	ds_read_u16 v75, v157
	s_waitcnt vmcnt(0)
	s_waitcnt lgkmcnt(0)
	s_waitcnt lgkmcnt(0)
	v_mov_b32_e32 v76, v166
	v_mov_b32_e32 v77, v167
	v_mov_b32_e32 v228, v74
	v_mov_b32_e32 v252, v75
	s_barrier
	v_mfma_scale_f32_16x16x128_f8f6f4 v[126:129], v[168:171], v[2:7], v[126:129], v161, v76 op_sel_hi:[0,0,0] cbsz:4 blgp:2
	v_mfma_scale_f32_16x16x128_f8f6f4 v[122:125], v[172:175], v[2:7], v[122:125], v161, v76 op_sel_hi:[0,0,0] cbsz:4 blgp:2
	v_mfma_scale_f32_16x16x128_f8f6f4 v[114:117], v[176:179], v[2:7], v[114:117], v161, v76 op_sel_hi:[0,0,0] cbsz:4 blgp:2
	v_mfma_scale_f32_16x16x128_f8f6f4 v[102:105], v[180:183], v[2:7], v[102:105], v161, v76 op_sel_hi:[0,0,0] cbsz:4 blgp:2
	v_mfma_scale_f32_16x16x128_f8f6f4 v[86:89], v[184:187], v[2:7], v[86:89], v161, v76 op_sel_hi:[0,0,0] cbsz:4 blgp:2
	v_mfma_scale_f32_16x16x128_f8f6f4 v[70:73], v[188:191], v[2:7], v[70:73], v161, v76 op_sel_hi:[0,0,0] cbsz:4 blgp:2
	v_mfma_scale_f32_16x16x128_f8f6f4 v[54:57], v[192:195], v[2:7], v[54:57], v161, v76 op_sel_hi:[0,0,0] cbsz:4 blgp:2
	v_mfma_scale_f32_16x16x128_f8f6f4 v[154:157], v[196:199], v[2:7], v[38:41], v161, v76 op_sel_hi:[0,0,0] cbsz:4 blgp:2
	v_mfma_scale_f32_16x16x128_f8f6f4 v[118:121], v[168:171], v[8:13], v[118:121], v161, v77 op_sel_hi:[0,0,0] cbsz:4 blgp:2
	v_mfma_scale_f32_16x16x128_f8f6f4 v[82:85], v[180:183], v[8:13], v[82:85], v161, v77 op_sel_hi:[0,0,0] cbsz:4 blgp:2
	v_mfma_scale_f32_16x16x128_f8f6f4 v[66:69], v[184:187], v[8:13], v[66:69], v161, v77 op_sel_hi:[0,0,0] cbsz:4 blgp:2
	v_mfma_scale_f32_16x16x128_f8f6f4 v[50:53], v[188:191], v[8:13], v[50:53], v161, v77 op_sel_hi:[0,0,0] cbsz:4 blgp:2
	v_mfma_scale_f32_16x16x128_f8f6f4 v[130:133], v[196:199], v[8:13], v[130:133], v161, v77 op_sel_hi:[0,0,0] cbsz:4 blgp:2
	v_mfma_scale_f32_16x16x128_f8f6f4 v[62:65], v[180:183], v[14:19], v[62:65], v161, v228 op_sel_hi:[0,0,0] cbsz:4 blgp:2
	v_mfma_scale_f32_16x16x128_f8f6f4 v[46:49], v[184:187], v[14:19], v[46:49], v161, v228 op_sel_hi:[0,0,0] cbsz:4 blgp:2
	v_mfma_scale_f32_16x16x128_f8f6f4 v[58:61], v[176:179], v[20:25], v[58:61], v161, v252 op_sel_hi:[0,0,0] cbsz:4 blgp:2
	v_mfma_scale_f32_16x16x128_f8f6f4 v[162:165], v[172:175], v[8:13], v[110:113], v161, v77 op_sel_hi:[0,0,0] cbsz:4 blgp:2
	v_mfma_scale_f32_16x16x128_f8f6f4 v[200:203], v[176:179], v[8:13], v[98:101], v161, v77 op_sel_hi:[0,0,0] cbsz:4 blgp:2
	v_mfma_scale_f32_16x16x128_f8f6f4 v[204:207], v[192:195], v[8:13], v[34:37], v161, v77 op_sel_hi:[0,0,0] cbsz:4 blgp:2
	v_mfma_scale_f32_16x16x128_f8f6f4 v[208:211], v[168:171], v[14:19], v[106:109], v161, v228 op_sel_hi:[0,0,0] cbsz:4 blgp:2
	v_mfma_scale_f32_16x16x128_f8f6f4 v[212:215], v[172:175], v[14:19], v[94:97], v161, v228 op_sel_hi:[0,0,0] cbsz:4 blgp:2
	v_mfma_scale_f32_16x16x128_f8f6f4 v[216:219], v[176:179], v[14:19], v[78:81], v161, v228 op_sel_hi:[0,0,0] cbsz:4 blgp:2
	v_mfma_scale_f32_16x16x128_f8f6f4 v[220:223], v[188:191], v[14:19], v[30:33], v161, v228 op_sel_hi:[0,0,0] cbsz:4 blgp:2
	v_mfma_scale_f32_16x16x128_f8f6f4 v[224:227], v[192:195], v[14:19], v[134:137], v161, v228 op_sel_hi:[0,0,0] cbsz:4 blgp:2
	v_mfma_scale_f32_16x16x128_f8f6f4 v[228:231], v[196:199], v[14:19], v[138:141], v161, v228 op_sel_hi:[0,0,0] cbsz:4 blgp:2
	v_mfma_scale_f32_16x16x128_f8f6f4 v[232:235], v[168:171], v[20:25], v[90:93], v161, v252 op_sel_hi:[0,0,0] cbsz:4 blgp:2
	v_mfma_scale_f32_16x16x128_f8f6f4 v[236:239], v[172:175], v[20:25], v[236:239], v161, v252 op_sel_hi:[0,0,0] cbsz:4 blgp:2
	v_mfma_scale_f32_16x16x128_f8f6f4 v[42:45], v[180:183], v[20:25], v[42:45], v161, v252 op_sel_hi:[0,0,0] cbsz:4 blgp:2
	v_mfma_scale_f32_16x16x128_f8f6f4 v[240:243], v[184:187], v[20:25], v[26:29], v161, v252 op_sel_hi:[0,0,0] cbsz:4 blgp:2
	v_mfma_scale_f32_16x16x128_f8f6f4 v[244:247], v[188:191], v[20:25], v[142:145], v161, v252 op_sel_hi:[0,0,0] cbsz:4 blgp:2
	v_mfma_scale_f32_16x16x128_f8f6f4 v[248:251], v[192:195], v[20:25], v[146:149], v161, v252 op_sel_hi:[0,0,0] cbsz:4 blgp:2
	v_mfma_scale_f32_16x16x128_f8f6f4 v[252:255], v[196:199], v[20:25], v[150:153], v161, v252 op_sel_hi:[0,0,0] cbsz:4 blgp:2
	s_barrier
	ds_read_b64 v[18:19], v1
	ds_read_b64 v[20:21], v1 offset:8
	ds_read_b64 v[22:23], v1 offset:16
	ds_read_b64 v[24:25], v160
	ds_read_b64 v[26:27], v160 offset:8
	ds_read_b64 v[28:29], v160 offset:16
	ds_read_b64 v[30:31], v159
	ds_read_b64 v[32:33], v159 offset:8
	ds_read_b64 v[34:35], v159 offset:16
	ds_read_b64 v[36:37], v158
	ds_read_b64 v[38:39], v158 offset:8
	ds_read_b64 v[40:41], v158 offset:16
	s_waitcnt lgkmcnt(0)
	v_lshrrev_b32_e32 v1, 8, v166
	v_lshrrev_b32_e32 v76, 8, v167
	v_lshrrev_b32_e32 v112, 8, v74
	v_lshrrev_b32_e32 v160, 8, v75
	s_barrier
	v_mfma_scale_f32_16x16x128_f8f6f4 v[14:17], v[168:171], v[18:23], v[126:129], v161, v1 op_sel_hi:[0,0,0] cbsz:4 blgp:2
	v_mfma_scale_f32_16x16x128_f8f6f4 v[10:13], v[172:175], v[18:23], v[122:125], v161, v1 op_sel_hi:[0,0,0] cbsz:4 blgp:2
	v_mfma_scale_f32_16x16x128_f8f6f4 v[6:9], v[176:179], v[18:23], v[114:117], v161, v1 op_sel_hi:[0,0,0] cbsz:4 blgp:2
	v_mfma_scale_f32_16x16x128_f8f6f4 v[2:5], v[180:183], v[18:23], v[102:105], v161, v1 op_sel_hi:[0,0,0] cbsz:4 blgp:2
	v_mfma_scale_f32_16x16x128_f8f6f4 v[108:111], v[184:187], v[18:23], v[86:89], v161, v1 op_sel_hi:[0,0,0] cbsz:4 blgp:2
	v_mfma_scale_f32_16x16x128_f8f6f4 v[104:107], v[188:191], v[18:23], v[70:73], v161, v1 op_sel_hi:[0,0,0] cbsz:4 blgp:2
	v_mfma_scale_f32_16x16x128_f8f6f4 v[100:103], v[192:195], v[18:23], v[54:57], v161, v1 op_sel_hi:[0,0,0] cbsz:4 blgp:2
	v_mfma_scale_f32_16x16x128_f8f6f4 v[96:99], v[196:199], v[18:23], v[154:157], v161, v1 op_sel_hi:[0,0,0] cbsz:4 blgp:2
	v_mfma_scale_f32_16x16x128_f8f6f4 v[156:159], v[168:171], v[24:29], v[118:121], v161, v76 op_sel_hi:[0,0,0] cbsz:4 blgp:2
	v_mfma_scale_f32_16x16x128_f8f6f4 v[152:155], v[172:175], v[24:29], v[162:165], v161, v76 op_sel_hi:[0,0,0] cbsz:4 blgp:2
	v_mfma_scale_f32_16x16x128_f8f6f4 v[148:151], v[176:179], v[24:29], v[200:203], v161, v76 op_sel_hi:[0,0,0] cbsz:4 blgp:2
	v_mfma_scale_f32_16x16x128_f8f6f4 v[144:147], v[180:183], v[24:29], v[82:85], v161, v76 op_sel_hi:[0,0,0] cbsz:4 blgp:2
	v_mfma_scale_f32_16x16x128_f8f6f4 v[92:95], v[184:187], v[24:29], v[66:69], v161, v76 op_sel_hi:[0,0,0] cbsz:4 blgp:2
	v_mfma_scale_f32_16x16x128_f8f6f4 v[88:91], v[188:191], v[24:29], v[50:53], v161, v76 op_sel_hi:[0,0,0] cbsz:4 blgp:2
	v_mfma_scale_f32_16x16x128_f8f6f4 v[84:87], v[192:195], v[24:29], v[204:207], v161, v76 op_sel_hi:[0,0,0] cbsz:4 blgp:2
	v_mfma_scale_f32_16x16x128_f8f6f4 v[80:83], v[196:199], v[24:29], v[130:133], v161, v76 op_sel_hi:[0,0,0] cbsz:4 blgp:2
	v_mfma_scale_f32_16x16x128_f8f6f4 v[140:143], v[168:171], v[30:35], v[208:211], v161, v112 op_sel_hi:[0,0,0] cbsz:4 blgp:2
	v_mfma_scale_f32_16x16x128_f8f6f4 v[136:139], v[172:175], v[30:35], v[212:215], v161, v112 op_sel_hi:[0,0,0] cbsz:4 blgp:2
	v_mfma_scale_f32_16x16x128_f8f6f4 v[132:135], v[176:179], v[30:35], v[216:219], v161, v112 op_sel_hi:[0,0,0] cbsz:4 blgp:2
	v_mfma_scale_f32_16x16x128_f8f6f4 v[128:131], v[180:183], v[30:35], v[62:65], v161, v112 op_sel_hi:[0,0,0] cbsz:4 blgp:2
	v_mfma_scale_f32_16x16x128_f8f6f4 v[76:79], v[184:187], v[30:35], v[46:49], v161, v112 op_sel_hi:[0,0,0] cbsz:4 blgp:2
	v_mfma_scale_f32_16x16x128_f8f6f4 v[72:75], v[188:191], v[30:35], v[220:223], v161, v112 op_sel_hi:[0,0,0] cbsz:4 blgp:2
	v_mfma_scale_f32_16x16x128_f8f6f4 v[68:71], v[192:195], v[30:35], v[224:227], v161, v112 op_sel_hi:[0,0,0] cbsz:4 blgp:2
	v_mfma_scale_f32_16x16x128_f8f6f4 v[64:67], v[196:199], v[30:35], v[228:231], v161, v112 op_sel_hi:[0,0,0] cbsz:4 blgp:2
	v_mfma_scale_f32_16x16x128_f8f6f4 v[124:127], v[168:171], v[36:41], v[232:235], v161, v160 op_sel_hi:[0,0,0] cbsz:4 blgp:2
	v_mfma_scale_f32_16x16x128_f8f6f4 v[120:123], v[172:175], v[36:41], v[236:239], v161, v160 op_sel_hi:[0,0,0] cbsz:4 blgp:2
	v_mfma_scale_f32_16x16x128_f8f6f4 v[116:119], v[176:179], v[36:41], v[58:61], v161, v160 op_sel_hi:[0,0,0] cbsz:4 blgp:2
	v_mfma_scale_f32_16x16x128_f8f6f4 v[112:115], v[180:183], v[36:41], v[42:45], v161, v160 op_sel_hi:[0,0,0] cbsz:4 blgp:2
	v_mfma_scale_f32_16x16x128_f8f6f4 v[60:63], v[184:187], v[36:41], v[240:243], v161, v160 op_sel_hi:[0,0,0] cbsz:4 blgp:2
	v_mfma_scale_f32_16x16x128_f8f6f4 v[56:59], v[188:191], v[36:41], v[244:247], v161, v160 op_sel_hi:[0,0,0] cbsz:4 blgp:2
	v_mfma_scale_f32_16x16x128_f8f6f4 v[52:55], v[192:195], v[36:41], v[248:251], v161, v160 op_sel_hi:[0,0,0] cbsz:4 blgp:2
	v_mfma_scale_f32_16x16x128_f8f6f4 v[48:51], v[196:199], v[36:41], v[252:255], v161, v160 op_sel_hi:[0,0,0] cbsz:4 blgp:2
	s_barrier
	s_cmpk_gt_u32 s33, 0xff
	s_cbranch_scc1 .LBB3_6
	s_barrier
